# v13 + code placement: the seven GEMM K-loop heads aligned to 64 bytes
# speedup vs baseline: 1.0061x; 1.0061x over previous
.LBB0_286:
	s_lshl_b32 s10, s51, 19
	s_add_u32 s10, s20, s10
	s_addc_u32 s11, s21, 0
	s_and_b64 s[16:17], s[4:5], exec
	s_cselect_b32 s54, s11, s31
	s_cselect_b32 s55, s10, s30
	s_lshl_b32 s14, s50, 19
	s_add_u32 s16, s15, s14
	s_addc_u32 s17, s26, 0
	s_and_b64 s[36:37], s[4:5], exec
	s_cselect_b32 s56, s17, s23
	s_cselect_b32 s57, s16, s22
	s_add_i32 s60, 0, 0x10000
	v_add_u32_e32 v198, s60, v196
	s_add_i32 s62, 0, 0x14000
	v_add_u32_e32 v199, s62, v196
	ds_read_b128 v[160:163], v198
	ds_read_b128 v[152:155], v198 offset:1024
	ds_read_b128 v[156:159], v198 offset:2048
	ds_read_b128 v[148:151], v198 offset:3072
	ds_read_b128 v[144:147], v199
	ds_read_b128 v[136:139], v199 offset:1024
	ds_read_b128 v[140:143], v199 offset:2048
	ds_read_b128 v[132:135], v199 offset:3072
	s_add_u32 s36, s30, 0x40080
	s_addc_u32 s37, s31, 0
	s_add_i32 s58, s41, 0xc000
	v_lshl_add_u64 v[174:175], s[36:37], 0, v[168:169]
	s_mov_b32 m0, s58
	s_add_i32 s59, s41, 0xe000
	ds_read_b128 v[178:181], v197
	ds_read_b128 v[182:185], v197 offset:1024
	ds_read_b128 v[190:193], v197 offset:2048
	ds_read_b128 v[200:203], v197 offset:3072
	ds_read_b128 v[204:207], v197 offset:4096
	ds_read_b128 v[208:211], v197 offset:5120
	ds_read_b128 v[212:215], v197 offset:6144
	ds_read_b128 v[216:219], v197 offset:7168
	global_load_lds_dwordx4 v[174:175], off
	v_lshl_add_u64 v[174:175], s[36:37], 0, v[166:167]
	s_mov_b32 m0, s59
	s_nop 0
	global_load_lds_dwordx4 v[174:175], off
	s_waitcnt vmcnt(8)
	s_waitcnt lgkmcnt(0)
	s_barrier
	s_setprio 1
	s_waitcnt lgkmcnt(0)
	v_mfma_f32_16x16x32_bf16 v[128:131], v[160:163], v[178:181], 0
	v_mfma_f32_16x16x32_bf16 v[124:127], v[156:159], v[178:181], 0
	v_mfma_f32_16x16x32_bf16 v[116:119], v[156:159], v[190:193], 0
	v_mfma_f32_16x16x32_bf16 v[120:123], v[160:163], v[190:193], 0
	v_mfma_f32_16x16x32_bf16 v[112:115], v[160:163], v[204:207], 0
	v_mfma_f32_16x16x32_bf16 v[108:111], v[156:159], v[204:207], 0
	v_mfma_f32_16x16x32_bf16 v[100:103], v[156:159], v[212:215], 0
	v_mfma_f32_16x16x32_bf16 v[104:107], v[160:163], v[212:215], 0
	s_nop 0
	v_mfma_f32_16x16x32_bf16 v[128:131], v[152:155], v[182:185], v[128:131]
	v_mfma_f32_16x16x32_bf16 v[124:127], v[148:151], v[182:185], v[124:127]
	v_mfma_f32_16x16x32_bf16 v[116:119], v[148:151], v[200:203], v[116:119]
	v_mfma_f32_16x16x32_bf16 v[120:123], v[152:155], v[200:203], v[120:123]
	v_mfma_f32_16x16x32_bf16 v[112:115], v[152:155], v[208:211], v[112:115]
	v_mfma_f32_16x16x32_bf16 v[108:111], v[148:151], v[208:211], v[108:111]
	v_mfma_f32_16x16x32_bf16 v[100:103], v[148:151], v[216:219], v[100:103]
	v_mfma_f32_16x16x32_bf16 v[104:107], v[152:155], v[216:219], v[104:107]
	s_setprio 0
	s_setprio 1
	v_mfma_f32_16x16x32_bf16 v[96:99], v[144:147], v[178:181], 0
	v_mfma_f32_16x16x32_bf16 v[92:95], v[140:143], v[178:181], 0
	v_mfma_f32_16x16x32_bf16 v[84:87], v[140:143], v[190:193], 0
	v_mfma_f32_16x16x32_bf16 v[88:91], v[144:147], v[190:193], 0
	v_mfma_f32_16x16x32_bf16 v[80:83], v[144:147], v[204:207], 0
	v_mfma_f32_16x16x32_bf16 v[76:79], v[140:143], v[204:207], 0
	v_mfma_f32_16x16x32_bf16 v[68:71], v[140:143], v[212:215], 0
	v_mfma_f32_16x16x32_bf16 v[72:75], v[144:147], v[212:215], 0
	s_nop 0
	v_mfma_f32_16x16x32_bf16 v[96:99], v[136:139], v[182:185], v[96:99]
	v_mfma_f32_16x16x32_bf16 v[92:95], v[132:135], v[182:185], v[92:95]
	v_mfma_f32_16x16x32_bf16 v[84:87], v[132:135], v[200:203], v[84:87]
	v_mfma_f32_16x16x32_bf16 v[88:91], v[136:139], v[200:203], v[88:91]
	v_mfma_f32_16x16x32_bf16 v[80:83], v[136:139], v[208:211], v[80:83]
	v_mfma_f32_16x16x32_bf16 v[76:79], v[132:135], v[208:211], v[76:79]
	v_mfma_f32_16x16x32_bf16 v[68:71], v[132:135], v[216:219], v[68:71]
	v_mfma_f32_16x16x32_bf16 v[72:75], v[136:139], v[216:219], v[72:75]
	s_setprio 0
	s_barrier
	v_lshl_add_u64 v[174:175], s[22:23], 0, v[34:35]
	s_add_i32 s60, s60, s40
	v_lshl_add_u64 v[190:191], v[174:175], 0, s[28:29]
	s_mov_b32 m0, s60
	s_add_i32 s61, s60, 0x2000
	ds_read_b128 v[178:181], v197 offset:16384
	ds_read_b128 v[182:185], v197 offset:17408
	ds_read_b128 v[200:203], v197 offset:18432
	ds_read_b128 v[204:207], v197 offset:19456
	ds_read_b128 v[208:211], v197 offset:20480
	ds_read_b128 v[212:215], v197 offset:21504
	ds_read_b128 v[216:219], v197 offset:22528
	ds_read_b128 v[222:225], v197 offset:23552
	global_load_lds_dwordx4 v[190:191], off
	v_lshl_add_u64 v[190:191], s[22:23], 0, v[164:165]
	s_add_u32 s36, s22, 0x40100
	v_lshl_add_u64 v[192:193], v[190:191], 0, s[28:29]
	s_mov_b32 m0, s61
	s_addc_u32 s37, s23, 0
	s_add_i32 s62, s62, s40
	global_load_lds_dwordx4 v[192:193], off
	v_lshl_add_u64 v[192:193], s[36:37], 0, v[34:35]
	s_mov_b32 m0, s62
	s_add_i32 s63, s62, 0x2000
	global_load_lds_dwordx4 v[192:193], off
	v_lshl_add_u64 v[192:193], s[36:37], 0, v[164:165]
	s_mov_b32 m0, s63
	s_nop 0
	global_load_lds_dwordx4 v[192:193], off
	v_lshl_add_u64 v[192:193], s[30:31], 0, v[168:169]
	v_lshl_add_u64 v[194:195], v[192:193], 0, s[28:29]
	s_mov_b32 m0, s41
	s_nop 0
	global_load_lds_dwordx4 v[194:195], off
	v_lshl_add_u64 v[194:195], s[30:31], 0, v[166:167]
	v_lshl_add_u64 v[226:227], v[194:195], 0, s[28:29]
	s_mov_b32 m0, s42
	s_nop 0
	global_load_lds_dwordx4 v[226:227], off
	s_waitcnt vmcnt(8)
	s_waitcnt lgkmcnt(0)
	s_barrier
	s_setprio 1
	s_waitcnt lgkmcnt(0)
	v_mfma_f32_16x16x32_bf16 v[64:67], v[160:163], v[178:181], 0
	v_mfma_f32_16x16x32_bf16 v[60:63], v[156:159], v[178:181], 0
	v_mfma_f32_16x16x32_bf16 v[52:55], v[156:159], v[200:203], 0
	v_mfma_f32_16x16x32_bf16 v[56:59], v[160:163], v[200:203], 0
	v_mfma_f32_16x16x32_bf16 v[48:51], v[160:163], v[208:211], 0
	v_mfma_f32_16x16x32_bf16 v[44:47], v[156:159], v[208:211], 0
	v_mfma_f32_16x16x32_bf16 v[36:39], v[156:159], v[216:219], 0
	v_mfma_f32_16x16x32_bf16 v[40:43], v[160:163], v[216:219], 0
	s_nop 0
	v_mfma_f32_16x16x32_bf16 v[64:67], v[152:155], v[182:185], v[64:67]
	v_mfma_f32_16x16x32_bf16 v[60:63], v[148:151], v[182:185], v[60:63]
	v_mfma_f32_16x16x32_bf16 v[52:55], v[148:151], v[204:207], v[52:55]
	v_mfma_f32_16x16x32_bf16 v[56:59], v[152:155], v[204:207], v[56:59]
	v_mfma_f32_16x16x32_bf16 v[48:51], v[152:155], v[212:215], v[48:51]
	v_mfma_f32_16x16x32_bf16 v[44:47], v[148:151], v[212:215], v[44:47]
	v_mfma_f32_16x16x32_bf16 v[36:39], v[148:151], v[222:225], v[36:39]
	v_mfma_f32_16x16x32_bf16 v[40:43], v[152:155], v[222:225], v[40:43]
	s_setprio 0
	s_setprio 1
	v_mfma_f32_16x16x32_bf16 v[30:33], v[144:147], v[178:181], 0
	v_mfma_f32_16x16x32_bf16 v[26:29], v[140:143], v[178:181], 0
	v_mfma_f32_16x16x32_bf16 v[18:21], v[140:143], v[200:203], 0
	v_mfma_f32_16x16x32_bf16 v[22:25], v[144:147], v[200:203], 0
	v_mfma_f32_16x16x32_bf16 v[14:17], v[144:147], v[208:211], 0
	v_mfma_f32_16x16x32_bf16 v[10:13], v[140:143], v[208:211], 0
	v_mfma_f32_16x16x32_bf16 v[2:5], v[140:143], v[216:219], 0
	v_mfma_f32_16x16x32_bf16 v[6:9], v[144:147], v[216:219], 0
	s_nop 0
	v_mfma_f32_16x16x32_bf16 v[30:33], v[136:139], v[182:185], v[30:33]
	v_mfma_f32_16x16x32_bf16 v[26:29], v[132:135], v[182:185], v[26:29]
	v_mfma_f32_16x16x32_bf16 v[18:21], v[132:135], v[204:207], v[18:21]
	v_mfma_f32_16x16x32_bf16 v[22:25], v[136:139], v[204:207], v[22:25]
	v_mfma_f32_16x16x32_bf16 v[14:17], v[136:139], v[212:215], v[14:17]
	v_mfma_f32_16x16x32_bf16 v[10:13], v[132:135], v[212:215], v[10:13]
	v_mfma_f32_16x16x32_bf16 v[2:5], v[132:135], v[222:225], v[2:5]
	v_mfma_f32_16x16x32_bf16 v[6:9], v[136:139], v[222:225], v[6:9]
	s_setprio 0
	s_barrier
	s_add_i32 s64, 0, 0x18000
	s_add_i32 s66, 0, 0x1c000
	v_add_u32_e32 v132, s64, v196
	v_add_u32_e32 v133, s66, v196
	ds_read_b128 v[134:137], v132
	ds_read_b128 v[138:141], v132 offset:1024
	ds_read_b128 v[142:145], v132 offset:2048
	ds_read_b128 v[146:149], v132 offset:3072
	ds_read_b128 v[150:153], v133
	ds_read_b128 v[154:157], v133 offset:1024
	ds_read_b128 v[158:161], v133 offset:2048
	ds_read_b128 v[178:181], v133 offset:3072
	s_add_u32 s36, s30, 0x40100
	s_addc_u32 s37, s31, 0
	s_mov_b32 m0, s43
	v_lshl_add_u64 v[162:163], s[36:37], 0, v[168:169]
	ds_read_b128 v[182:185], v197 offset:32768
	ds_read_b128 v[200:203], v197 offset:33792
	ds_read_b128 v[204:207], v197 offset:34816
	ds_read_b128 v[208:211], v197 offset:35840
	ds_read_b128 v[212:215], v197 offset:36864
	ds_read_b128 v[216:219], v197 offset:37888
	ds_read_b128 v[222:225], v197 offset:38912
	ds_read_b128 v[226:229], v197 offset:39936
	global_load_lds_dwordx4 v[162:163], off
	v_lshl_add_u64 v[162:163], s[36:37], 0, v[166:167]
	s_mov_b32 m0, s44
	s_nop 0
	global_load_lds_dwordx4 v[162:163], off
	s_waitcnt vmcnt(8)
	s_waitcnt lgkmcnt(0)
	s_barrier
	s_setprio 1
	s_waitcnt lgkmcnt(0)
	v_mfma_f32_16x16x32_bf16 v[128:131], v[134:137], v[182:185], v[128:131]
	v_mfma_f32_16x16x32_bf16 v[124:127], v[142:145], v[182:185], v[124:127]
	v_mfma_f32_16x16x32_bf16 v[116:119], v[142:145], v[204:207], v[116:119]
	v_mfma_f32_16x16x32_bf16 v[120:123], v[134:137], v[204:207], v[120:123]
	v_mfma_f32_16x16x32_bf16 v[112:115], v[134:137], v[212:215], v[112:115]
	v_mfma_f32_16x16x32_bf16 v[108:111], v[142:145], v[212:215], v[108:111]
	v_mfma_f32_16x16x32_bf16 v[100:103], v[142:145], v[222:225], v[100:103]
	v_mfma_f32_16x16x32_bf16 v[104:107], v[134:137], v[222:225], v[104:107]
	v_mfma_f32_16x16x32_bf16 v[128:131], v[138:141], v[200:203], v[128:131]
	v_mfma_f32_16x16x32_bf16 v[124:127], v[146:149], v[200:203], v[124:127]
	v_mfma_f32_16x16x32_bf16 v[116:119], v[146:149], v[208:211], v[116:119]
	v_mfma_f32_16x16x32_bf16 v[120:123], v[138:141], v[208:211], v[120:123]
	v_mfma_f32_16x16x32_bf16 v[112:115], v[138:141], v[216:219], v[112:115]
	v_mfma_f32_16x16x32_bf16 v[108:111], v[146:149], v[216:219], v[108:111]
	v_mfma_f32_16x16x32_bf16 v[100:103], v[146:149], v[226:229], v[100:103]
	v_mfma_f32_16x16x32_bf16 v[104:107], v[138:141], v[226:229], v[104:107]
	s_setprio 0
	s_setprio 1
	v_mfma_f32_16x16x32_bf16 v[96:99], v[150:153], v[182:185], v[96:99]
	v_mfma_f32_16x16x32_bf16 v[92:95], v[158:161], v[182:185], v[92:95]
	v_mfma_f32_16x16x32_bf16 v[84:87], v[158:161], v[204:207], v[84:87]
	v_mfma_f32_16x16x32_bf16 v[88:91], v[150:153], v[204:207], v[88:91]
	v_mfma_f32_16x16x32_bf16 v[80:83], v[150:153], v[212:215], v[80:83]
	v_mfma_f32_16x16x32_bf16 v[76:79], v[158:161], v[212:215], v[76:79]
	v_mfma_f32_16x16x32_bf16 v[68:71], v[158:161], v[222:225], v[68:71]
	v_mfma_f32_16x16x32_bf16 v[72:75], v[150:153], v[222:225], v[72:75]
	v_mfma_f32_16x16x32_bf16 v[96:99], v[154:157], v[200:203], v[96:99]
	v_mfma_f32_16x16x32_bf16 v[92:95], v[178:181], v[200:203], v[92:95]
	v_mfma_f32_16x16x32_bf16 v[84:87], v[178:181], v[208:211], v[84:87]
	v_mfma_f32_16x16x32_bf16 v[88:91], v[154:157], v[208:211], v[88:91]
	v_mfma_f32_16x16x32_bf16 v[80:83], v[154:157], v[216:219], v[80:83]
	v_mfma_f32_16x16x32_bf16 v[76:79], v[178:181], v[216:219], v[76:79]
	v_mfma_f32_16x16x32_bf16 v[68:71], v[178:181], v[226:229], v[68:71]
	v_mfma_f32_16x16x32_bf16 v[72:75], v[154:157], v[226:229], v[72:75]
	s_setprio 0
	s_barrier
	s_add_i32 s64, s64, s40
	s_mov_b64 s[24:25], 0x180
	s_add_i32 s65, s64, 0x2000
	v_lshl_add_u64 v[162:163], v[174:175], 0, s[24:25]
	s_mov_b32 m0, s64
	s_add_u32 s36, s22, 0x40180
	ds_read_b128 v[182:185], v197 offset:49152
	ds_read_b128 v[200:203], v197 offset:50176
	ds_read_b128 v[204:207], v197 offset:51200
	ds_read_b128 v[208:211], v197 offset:52224
	ds_read_b128 v[212:215], v197 offset:53248
	ds_read_b128 v[216:219], v197 offset:54272
	ds_read_b128 v[222:225], v197 offset:55296
	ds_read_b128 v[226:229], v197 offset:56320
	global_load_lds_dwordx4 v[162:163], off
	v_lshl_add_u64 v[162:163], v[190:191], 0, s[24:25]
	s_mov_b32 m0, s65
	s_addc_u32 s37, s23, 0
	s_add_i32 s66, s66, s40
	global_load_lds_dwordx4 v[162:163], off
	v_lshl_add_u64 v[162:163], s[36:37], 0, v[34:35]
	s_mov_b32 m0, s66
	s_add_i32 s67, s66, 0x2000
	global_load_lds_dwordx4 v[162:163], off
	v_lshl_add_u64 v[162:163], s[36:37], 0, v[164:165]
	s_mov_b32 m0, s67
	s_nop 0
	global_load_lds_dwordx4 v[162:163], off
	v_lshl_add_u64 v[162:163], v[192:193], 0, s[24:25]
	s_mov_b32 m0, s47
	s_nop 0
	global_load_lds_dwordx4 v[162:163], off
	v_lshl_add_u64 v[162:163], v[194:195], 0, s[24:25]
	s_mov_b32 m0, s48
	s_nop 0
	global_load_lds_dwordx4 v[162:163], off
	s_waitcnt vmcnt(8)
	s_waitcnt lgkmcnt(0)
	s_barrier
	s_setprio 1
	s_waitcnt lgkmcnt(0)
	v_mfma_f32_16x16x32_bf16 v[64:67], v[134:137], v[182:185], v[64:67]
	v_mfma_f32_16x16x32_bf16 v[60:63], v[142:145], v[182:185], v[60:63]
	v_mfma_f32_16x16x32_bf16 v[52:55], v[142:145], v[204:207], v[52:55]
	v_mfma_f32_16x16x32_bf16 v[56:59], v[134:137], v[204:207], v[56:59]
	v_mfma_f32_16x16x32_bf16 v[48:51], v[134:137], v[212:215], v[48:51]
	v_mfma_f32_16x16x32_bf16 v[44:47], v[142:145], v[212:215], v[44:47]
	v_mfma_f32_16x16x32_bf16 v[36:39], v[142:145], v[222:225], v[36:39]
	v_mfma_f32_16x16x32_bf16 v[40:43], v[134:137], v[222:225], v[40:43]
	v_mfma_f32_16x16x32_bf16 v[64:67], v[138:141], v[200:203], v[64:67]
	v_mfma_f32_16x16x32_bf16 v[60:63], v[146:149], v[200:203], v[60:63]
	v_mfma_f32_16x16x32_bf16 v[52:55], v[146:149], v[208:211], v[52:55]
	v_mfma_f32_16x16x32_bf16 v[56:59], v[138:141], v[208:211], v[56:59]
	v_mfma_f32_16x16x32_bf16 v[48:51], v[138:141], v[216:219], v[48:51]
	v_mfma_f32_16x16x32_bf16 v[44:47], v[146:149], v[216:219], v[44:47]
	v_mfma_f32_16x16x32_bf16 v[36:39], v[146:149], v[226:229], v[36:39]
	v_mfma_f32_16x16x32_bf16 v[40:43], v[138:141], v[226:229], v[40:43]
	s_setprio 0
	s_setprio 1
	v_mfma_f32_16x16x32_bf16 v[30:33], v[150:153], v[182:185], v[30:33]
	v_mfma_f32_16x16x32_bf16 v[26:29], v[158:161], v[182:185], v[26:29]
	v_mfma_f32_16x16x32_bf16 v[18:21], v[158:161], v[204:207], v[18:21]
	v_mfma_f32_16x16x32_bf16 v[22:25], v[150:153], v[204:207], v[22:25]
	v_mfma_f32_16x16x32_bf16 v[14:17], v[150:153], v[212:215], v[14:17]
	v_mfma_f32_16x16x32_bf16 v[10:13], v[158:161], v[212:215], v[10:13]
	v_mfma_f32_16x16x32_bf16 v[2:5], v[158:161], v[222:225], v[2:5]
	v_mfma_f32_16x16x32_bf16 v[6:9], v[150:153], v[222:225], v[6:9]
	v_mfma_f32_16x16x32_bf16 v[30:33], v[154:157], v[200:203], v[30:33]
	v_mfma_f32_16x16x32_bf16 v[26:29], v[178:181], v[200:203], v[26:29]
	v_mfma_f32_16x16x32_bf16 v[18:21], v[178:181], v[208:211], v[18:21]
	v_mfma_f32_16x16x32_bf16 v[22:25], v[154:157], v[208:211], v[22:25]
	v_mfma_f32_16x16x32_bf16 v[14:17], v[154:157], v[216:219], v[14:17]
	v_mfma_f32_16x16x32_bf16 v[10:13], v[178:181], v[216:219], v[10:13]
	v_mfma_f32_16x16x32_bf16 v[2:5], v[178:181], v[226:229], v[2:5]
	v_mfma_f32_16x16x32_bf16 v[6:9], v[154:157], v[226:229], v[6:9]
	s_setprio 0
	s_barrier
	s_add_u32 s30, s30, 0x40180
	s_addc_u32 s31, s31, 0
	s_add_u32 s68, s22, 0x200
	s_addc_u32 s69, s23, 0
	s_mov_b32 s70, 0
	.p2align	6

.LBB0_540:
	s_lshl_b32 s14, s55, 19
	v_readlane_b32 s16, v253, 53
	v_readlane_b32 s17, v253, 54
	s_add_u32 s16, s16, s14
	s_addc_u32 s17, s17, 0
	s_and_b64 s[22:23], s[4:5], exec
	s_cselect_b32 s58, s17, s37
	s_cselect_b32 s59, s16, s36
	s_lshl_b32 s14, s54, 19
	s_add_u32 s22, s15, s14
	s_addc_u32 s23, s26, 0
	s_and_b64 s[40:41], s[4:5], exec
	s_cselect_b32 s60, s23, s31
	s_cselect_b32 s61, s22, s30
	s_add_i32 s64, 0, 0x10000
	v_add_u32_e32 v172, s64, v222
	s_add_i32 s66, 0, 0x14000
	v_add_u32_e32 v173, s66, v222
	ds_read_b128 v[160:163], v172
	ds_read_b128 v[152:155], v172 offset:1024
	ds_read_b128 v[156:159], v172 offset:2048
	ds_read_b128 v[148:151], v172 offset:3072
	ds_read_b128 v[144:147], v173
	ds_read_b128 v[136:139], v173 offset:1024
	ds_read_b128 v[140:143], v173 offset:2048
	ds_read_b128 v[132:135], v173 offset:3072
	s_add_u32 s40, s36, 0x40080
	s_addc_u32 s41, s37, 0
	s_add_i32 s62, s43, 0xc000
	v_lshl_add_u64 v[174:175], s[40:41], 0, v[194:195]
	s_mov_b32 m0, s62
	s_add_i32 s63, s43, 0xe000
	ds_read_b128 v[164:167], v223
	ds_read_b128 v[168:171], v223 offset:1024
	ds_read_b128 v[178:181], v223 offset:2048
	ds_read_b128 v[182:185], v223 offset:3072
	ds_read_b128 v[200:203], v223 offset:4096
	ds_read_b128 v[204:207], v223 offset:5120
	ds_read_b128 v[208:211], v223 offset:6144
	ds_read_b128 v[212:215], v223 offset:7168
	global_load_lds_dwordx4 v[174:175], off
	v_lshl_add_u64 v[174:175], s[40:41], 0, v[192:193]
	s_mov_b32 m0, s63
	s_nop 0
	global_load_lds_dwordx4 v[174:175], off
	s_waitcnt vmcnt(8)
	s_waitcnt lgkmcnt(0)
	s_barrier
	s_setprio 1
	s_waitcnt lgkmcnt(0)
	v_mfma_f32_16x16x32_bf16 v[128:131], v[160:163], v[164:167], 0
	v_mfma_f32_16x16x32_bf16 v[124:127], v[156:159], v[164:167], 0
	v_mfma_f32_16x16x32_bf16 v[116:119], v[156:159], v[178:181], 0
	v_mfma_f32_16x16x32_bf16 v[120:123], v[160:163], v[178:181], 0
	v_mfma_f32_16x16x32_bf16 v[112:115], v[160:163], v[200:203], 0
	v_mfma_f32_16x16x32_bf16 v[108:111], v[156:159], v[200:203], 0
	v_mfma_f32_16x16x32_bf16 v[100:103], v[156:159], v[208:211], 0
	v_mfma_f32_16x16x32_bf16 v[104:107], v[160:163], v[208:211], 0
	s_nop 0
	v_mfma_f32_16x16x32_bf16 v[128:131], v[152:155], v[168:171], v[128:131]
	v_mfma_f32_16x16x32_bf16 v[124:127], v[148:151], v[168:171], v[124:127]
	v_mfma_f32_16x16x32_bf16 v[116:119], v[148:151], v[182:185], v[116:119]
	v_mfma_f32_16x16x32_bf16 v[120:123], v[152:155], v[182:185], v[120:123]
	v_mfma_f32_16x16x32_bf16 v[112:115], v[152:155], v[204:207], v[112:115]
	v_mfma_f32_16x16x32_bf16 v[108:111], v[148:151], v[204:207], v[108:111]
	v_mfma_f32_16x16x32_bf16 v[100:103], v[148:151], v[212:215], v[100:103]
	v_mfma_f32_16x16x32_bf16 v[104:107], v[152:155], v[212:215], v[104:107]
	s_setprio 0
	s_setprio 1
	v_mfma_f32_16x16x32_bf16 v[96:99], v[144:147], v[164:167], 0
	v_mfma_f32_16x16x32_bf16 v[92:95], v[140:143], v[164:167], 0
	v_mfma_f32_16x16x32_bf16 v[84:87], v[140:143], v[178:181], 0
	v_mfma_f32_16x16x32_bf16 v[88:91], v[144:147], v[178:181], 0
	v_mfma_f32_16x16x32_bf16 v[80:83], v[144:147], v[200:203], 0
	v_mfma_f32_16x16x32_bf16 v[76:79], v[140:143], v[200:203], 0
	v_mfma_f32_16x16x32_bf16 v[68:71], v[140:143], v[208:211], 0
	v_mfma_f32_16x16x32_bf16 v[72:75], v[144:147], v[208:211], 0
	s_nop 0
	v_mfma_f32_16x16x32_bf16 v[96:99], v[136:139], v[168:171], v[96:99]
	v_mfma_f32_16x16x32_bf16 v[92:95], v[132:135], v[168:171], v[92:95]
	v_mfma_f32_16x16x32_bf16 v[84:87], v[132:135], v[182:185], v[84:87]
	v_mfma_f32_16x16x32_bf16 v[88:91], v[136:139], v[182:185], v[88:91]
	v_mfma_f32_16x16x32_bf16 v[80:83], v[136:139], v[204:207], v[80:83]
	v_mfma_f32_16x16x32_bf16 v[76:79], v[132:135], v[204:207], v[76:79]
	v_mfma_f32_16x16x32_bf16 v[68:71], v[132:135], v[212:215], v[68:71]
	v_mfma_f32_16x16x32_bf16 v[72:75], v[136:139], v[212:215], v[72:75]
	s_setprio 0
	s_barrier
	v_lshl_add_u64 v[164:165], s[30:31], 0, v[34:35]
	s_add_i32 s64, s64, s42
	v_lshl_add_u64 v[166:167], v[164:165], 0, s[28:29]
	s_mov_b32 m0, s64
	s_add_i32 s65, s64, 0x2000
	ds_read_b128 v[178:181], v223 offset:16384
	ds_read_b128 v[182:185], v223 offset:17408
	ds_read_b128 v[200:203], v223 offset:18432
	ds_read_b128 v[204:207], v223 offset:19456
	ds_read_b128 v[208:211], v223 offset:20480
	ds_read_b128 v[212:215], v223 offset:21504
	ds_read_b128 v[216:219], v223 offset:22528
	ds_read_b128 v[224:227], v223 offset:23552
	global_load_lds_dwordx4 v[166:167], off
	v_lshl_add_u64 v[166:167], s[30:31], 0, v[190:191]
	s_add_u32 s40, s30, 0x40100
	v_lshl_add_u64 v[168:169], v[166:167], 0, s[28:29]
	s_mov_b32 m0, s65
	s_addc_u32 s41, s31, 0
	s_add_i32 s66, s66, s42
	global_load_lds_dwordx4 v[168:169], off
	v_lshl_add_u64 v[168:169], s[40:41], 0, v[34:35]
	s_mov_b32 m0, s66
	s_add_i32 s67, s66, 0x2000
	global_load_lds_dwordx4 v[168:169], off
	v_lshl_add_u64 v[168:169], s[40:41], 0, v[190:191]
	s_mov_b32 m0, s67
	s_nop 0
	global_load_lds_dwordx4 v[168:169], off
	v_lshl_add_u64 v[168:169], s[36:37], 0, v[194:195]
	v_lshl_add_u64 v[170:171], v[168:169], 0, s[28:29]
	s_mov_b32 m0, s43
	s_nop 0
	global_load_lds_dwordx4 v[170:171], off
	v_lshl_add_u64 v[170:171], s[36:37], 0, v[192:193]
	v_lshl_add_u64 v[174:175], v[170:171], 0, s[28:29]
	s_mov_b32 m0, s44
	s_nop 0
	global_load_lds_dwordx4 v[174:175], off
	s_waitcnt vmcnt(8)
	s_waitcnt lgkmcnt(0)
	s_barrier
	s_setprio 1
	s_waitcnt lgkmcnt(0)
	v_mfma_f32_16x16x32_bf16 v[64:67], v[160:163], v[178:181], 0
	v_mfma_f32_16x16x32_bf16 v[60:63], v[156:159], v[178:181], 0
	v_mfma_f32_16x16x32_bf16 v[52:55], v[156:159], v[200:203], 0
	v_mfma_f32_16x16x32_bf16 v[56:59], v[160:163], v[200:203], 0
	v_mfma_f32_16x16x32_bf16 v[48:51], v[160:163], v[208:211], 0
	v_mfma_f32_16x16x32_bf16 v[44:47], v[156:159], v[208:211], 0
	v_mfma_f32_16x16x32_bf16 v[36:39], v[156:159], v[216:219], 0
	v_mfma_f32_16x16x32_bf16 v[40:43], v[160:163], v[216:219], 0
	s_nop 0
	v_mfma_f32_16x16x32_bf16 v[64:67], v[152:155], v[182:185], v[64:67]
	v_mfma_f32_16x16x32_bf16 v[60:63], v[148:151], v[182:185], v[60:63]
	v_mfma_f32_16x16x32_bf16 v[52:55], v[148:151], v[204:207], v[52:55]
	v_mfma_f32_16x16x32_bf16 v[56:59], v[152:155], v[204:207], v[56:59]
	v_mfma_f32_16x16x32_bf16 v[48:51], v[152:155], v[212:215], v[48:51]
	v_mfma_f32_16x16x32_bf16 v[44:47], v[148:151], v[212:215], v[44:47]
	v_mfma_f32_16x16x32_bf16 v[36:39], v[148:151], v[224:227], v[36:39]
	v_mfma_f32_16x16x32_bf16 v[40:43], v[152:155], v[224:227], v[40:43]
	s_setprio 0
	s_setprio 1
	v_mfma_f32_16x16x32_bf16 v[30:33], v[144:147], v[178:181], 0
	v_mfma_f32_16x16x32_bf16 v[26:29], v[140:143], v[178:181], 0
	v_mfma_f32_16x16x32_bf16 v[18:21], v[140:143], v[200:203], 0
	v_mfma_f32_16x16x32_bf16 v[22:25], v[144:147], v[200:203], 0
	v_mfma_f32_16x16x32_bf16 v[14:17], v[144:147], v[208:211], 0
	v_mfma_f32_16x16x32_bf16 v[10:13], v[140:143], v[208:211], 0
	v_mfma_f32_16x16x32_bf16 v[2:5], v[140:143], v[216:219], 0
	v_mfma_f32_16x16x32_bf16 v[6:9], v[144:147], v[216:219], 0
	s_nop 0
	v_mfma_f32_16x16x32_bf16 v[30:33], v[136:139], v[182:185], v[30:33]
	v_mfma_f32_16x16x32_bf16 v[26:29], v[132:135], v[182:185], v[26:29]
	v_mfma_f32_16x16x32_bf16 v[18:21], v[132:135], v[204:207], v[18:21]
	v_mfma_f32_16x16x32_bf16 v[22:25], v[136:139], v[204:207], v[22:25]
	v_mfma_f32_16x16x32_bf16 v[14:17], v[136:139], v[212:215], v[14:17]
	v_mfma_f32_16x16x32_bf16 v[10:13], v[132:135], v[212:215], v[10:13]
	v_mfma_f32_16x16x32_bf16 v[2:5], v[132:135], v[224:227], v[2:5]
	v_mfma_f32_16x16x32_bf16 v[6:9], v[136:139], v[224:227], v[6:9]
	s_setprio 0
	s_barrier
	s_add_i32 s68, 0, 0x18000
	s_add_i32 s70, 0, 0x1c000
	v_add_u32_e32 v132, s68, v222
	v_add_u32_e32 v133, s70, v222
	ds_read_b128 v[134:137], v132
	ds_read_b128 v[138:141], v132 offset:1024
	ds_read_b128 v[142:145], v132 offset:2048
	ds_read_b128 v[146:149], v132 offset:3072
	ds_read_b128 v[150:153], v133
	ds_read_b128 v[154:157], v133 offset:1024
	ds_read_b128 v[158:161], v133 offset:2048
	ds_read_b128 v[178:181], v133 offset:3072
	s_add_u32 s40, s36, 0x40100
	s_addc_u32 s41, s37, 0
	s_mov_b32 m0, s45
	v_lshl_add_u64 v[162:163], s[40:41], 0, v[194:195]
	ds_read_b128 v[182:185], v223 offset:32768
	ds_read_b128 v[200:203], v223 offset:33792
	ds_read_b128 v[204:207], v223 offset:34816
	ds_read_b128 v[208:211], v223 offset:35840
	ds_read_b128 v[212:215], v223 offset:36864
	ds_read_b128 v[216:219], v223 offset:37888
	ds_read_b128 v[224:227], v223 offset:38912
	ds_read_b128 v[228:231], v223 offset:39936
	global_load_lds_dwordx4 v[162:163], off
	v_lshl_add_u64 v[162:163], s[40:41], 0, v[192:193]
	s_mov_b32 m0, s46
	s_nop 0
	global_load_lds_dwordx4 v[162:163], off
	s_waitcnt vmcnt(8)
	s_waitcnt lgkmcnt(0)
	s_barrier
	s_setprio 1
	s_waitcnt lgkmcnt(0)
	v_mfma_f32_16x16x32_bf16 v[128:131], v[134:137], v[182:185], v[128:131]
	v_mfma_f32_16x16x32_bf16 v[124:127], v[142:145], v[182:185], v[124:127]
	v_mfma_f32_16x16x32_bf16 v[116:119], v[142:145], v[204:207], v[116:119]
	v_mfma_f32_16x16x32_bf16 v[120:123], v[134:137], v[204:207], v[120:123]
	v_mfma_f32_16x16x32_bf16 v[112:115], v[134:137], v[212:215], v[112:115]
	v_mfma_f32_16x16x32_bf16 v[108:111], v[142:145], v[212:215], v[108:111]
	v_mfma_f32_16x16x32_bf16 v[100:103], v[142:145], v[224:227], v[100:103]
	v_mfma_f32_16x16x32_bf16 v[104:107], v[134:137], v[224:227], v[104:107]
	v_mfma_f32_16x16x32_bf16 v[128:131], v[138:141], v[200:203], v[128:131]
	v_mfma_f32_16x16x32_bf16 v[124:127], v[146:149], v[200:203], v[124:127]
	v_mfma_f32_16x16x32_bf16 v[116:119], v[146:149], v[208:211], v[116:119]
	v_mfma_f32_16x16x32_bf16 v[120:123], v[138:141], v[208:211], v[120:123]
	v_mfma_f32_16x16x32_bf16 v[112:115], v[138:141], v[216:219], v[112:115]
	v_mfma_f32_16x16x32_bf16 v[108:111], v[146:149], v[216:219], v[108:111]
	v_mfma_f32_16x16x32_bf16 v[100:103], v[146:149], v[228:231], v[100:103]
	v_mfma_f32_16x16x32_bf16 v[104:107], v[138:141], v[228:231], v[104:107]
	s_setprio 0
	s_setprio 1
	v_mfma_f32_16x16x32_bf16 v[96:99], v[150:153], v[182:185], v[96:99]
	v_mfma_f32_16x16x32_bf16 v[92:95], v[158:161], v[182:185], v[92:95]
	v_mfma_f32_16x16x32_bf16 v[84:87], v[158:161], v[204:207], v[84:87]
	v_mfma_f32_16x16x32_bf16 v[88:91], v[150:153], v[204:207], v[88:91]
	v_mfma_f32_16x16x32_bf16 v[80:83], v[150:153], v[212:215], v[80:83]
	v_mfma_f32_16x16x32_bf16 v[76:79], v[158:161], v[212:215], v[76:79]
	v_mfma_f32_16x16x32_bf16 v[68:71], v[158:161], v[224:227], v[68:71]
	v_mfma_f32_16x16x32_bf16 v[72:75], v[150:153], v[224:227], v[72:75]
	v_mfma_f32_16x16x32_bf16 v[96:99], v[154:157], v[200:203], v[96:99]
	v_mfma_f32_16x16x32_bf16 v[92:95], v[178:181], v[200:203], v[92:95]
	v_mfma_f32_16x16x32_bf16 v[84:87], v[178:181], v[208:211], v[84:87]
	v_mfma_f32_16x16x32_bf16 v[88:91], v[154:157], v[208:211], v[88:91]
	v_mfma_f32_16x16x32_bf16 v[80:83], v[154:157], v[216:219], v[80:83]
	v_mfma_f32_16x16x32_bf16 v[76:79], v[178:181], v[216:219], v[76:79]
	v_mfma_f32_16x16x32_bf16 v[68:71], v[178:181], v[228:231], v[68:71]
	v_mfma_f32_16x16x32_bf16 v[72:75], v[154:157], v[228:231], v[72:75]
	s_setprio 0
	s_barrier
	s_add_i32 s68, s68, s42
	s_mov_b64 s[24:25], 0x180
	s_add_i32 s69, s68, 0x2000
	v_lshl_add_u64 v[162:163], v[164:165], 0, s[24:25]
	s_mov_b32 m0, s68
	s_add_u32 s40, s30, 0x40180
	ds_read_b128 v[182:185], v223 offset:49152
	ds_read_b128 v[200:203], v223 offset:50176
	ds_read_b128 v[204:207], v223 offset:51200
	ds_read_b128 v[208:211], v223 offset:52224
	ds_read_b128 v[212:215], v223 offset:53248
	ds_read_b128 v[216:219], v223 offset:54272
	ds_read_b128 v[224:227], v223 offset:55296
	ds_read_b128 v[228:231], v223 offset:56320
	global_load_lds_dwordx4 v[162:163], off
	v_lshl_add_u64 v[162:163], v[166:167], 0, s[24:25]
	s_mov_b32 m0, s69
	s_addc_u32 s41, s31, 0
	s_add_i32 s70, s70, s42
	global_load_lds_dwordx4 v[162:163], off
	v_lshl_add_u64 v[162:163], s[40:41], 0, v[34:35]
	s_mov_b32 m0, s70
	s_add_i32 s71, s70, 0x2000
	global_load_lds_dwordx4 v[162:163], off
	v_lshl_add_u64 v[162:163], s[40:41], 0, v[190:191]
	s_mov_b32 m0, s71
	s_nop 0
	global_load_lds_dwordx4 v[162:163], off
	v_lshl_add_u64 v[162:163], v[168:169], 0, s[24:25]
	s_mov_b32 m0, s51
	s_nop 0
	global_load_lds_dwordx4 v[162:163], off
	v_lshl_add_u64 v[162:163], v[170:171], 0, s[24:25]
	s_mov_b32 m0, s52
	s_nop 0
	global_load_lds_dwordx4 v[162:163], off
	s_waitcnt vmcnt(8)
	s_waitcnt lgkmcnt(0)
	s_barrier
	s_setprio 1
	s_waitcnt lgkmcnt(0)
	v_mfma_f32_16x16x32_bf16 v[64:67], v[134:137], v[182:185], v[64:67]
	v_mfma_f32_16x16x32_bf16 v[60:63], v[142:145], v[182:185], v[60:63]
	v_mfma_f32_16x16x32_bf16 v[52:55], v[142:145], v[204:207], v[52:55]
	v_mfma_f32_16x16x32_bf16 v[56:59], v[134:137], v[204:207], v[56:59]
	v_mfma_f32_16x16x32_bf16 v[48:51], v[134:137], v[212:215], v[48:51]
	v_mfma_f32_16x16x32_bf16 v[44:47], v[142:145], v[212:215], v[44:47]
	v_mfma_f32_16x16x32_bf16 v[36:39], v[142:145], v[224:227], v[36:39]
	v_mfma_f32_16x16x32_bf16 v[40:43], v[134:137], v[224:227], v[40:43]
	v_mfma_f32_16x16x32_bf16 v[64:67], v[138:141], v[200:203], v[64:67]
	v_mfma_f32_16x16x32_bf16 v[60:63], v[146:149], v[200:203], v[60:63]
	v_mfma_f32_16x16x32_bf16 v[52:55], v[146:149], v[208:211], v[52:55]
	v_mfma_f32_16x16x32_bf16 v[56:59], v[138:141], v[208:211], v[56:59]
	v_mfma_f32_16x16x32_bf16 v[48:51], v[138:141], v[216:219], v[48:51]
	v_mfma_f32_16x16x32_bf16 v[44:47], v[146:149], v[216:219], v[44:47]
	v_mfma_f32_16x16x32_bf16 v[36:39], v[146:149], v[228:231], v[36:39]
	v_mfma_f32_16x16x32_bf16 v[40:43], v[138:141], v[228:231], v[40:43]
	s_setprio 0
	s_setprio 1
	v_mfma_f32_16x16x32_bf16 v[30:33], v[150:153], v[182:185], v[30:33]
	v_mfma_f32_16x16x32_bf16 v[26:29], v[158:161], v[182:185], v[26:29]
	v_mfma_f32_16x16x32_bf16 v[18:21], v[158:161], v[204:207], v[18:21]
	v_mfma_f32_16x16x32_bf16 v[22:25], v[150:153], v[204:207], v[22:25]
	v_mfma_f32_16x16x32_bf16 v[14:17], v[150:153], v[212:215], v[14:17]
	v_mfma_f32_16x16x32_bf16 v[10:13], v[158:161], v[212:215], v[10:13]
	v_mfma_f32_16x16x32_bf16 v[2:5], v[158:161], v[224:227], v[2:5]
	v_mfma_f32_16x16x32_bf16 v[6:9], v[150:153], v[224:227], v[6:9]
	v_mfma_f32_16x16x32_bf16 v[30:33], v[154:157], v[200:203], v[30:33]
	v_mfma_f32_16x16x32_bf16 v[26:29], v[178:181], v[200:203], v[26:29]
	v_mfma_f32_16x16x32_bf16 v[18:21], v[178:181], v[208:211], v[18:21]
	v_mfma_f32_16x16x32_bf16 v[22:25], v[154:157], v[208:211], v[22:25]
	v_mfma_f32_16x16x32_bf16 v[14:17], v[154:157], v[216:219], v[14:17]
	v_mfma_f32_16x16x32_bf16 v[10:13], v[178:181], v[216:219], v[10:13]
	v_mfma_f32_16x16x32_bf16 v[2:5], v[178:181], v[228:231], v[2:5]
	v_mfma_f32_16x16x32_bf16 v[6:9], v[154:157], v[228:231], v[6:9]
	s_setprio 0
	s_barrier
	s_add_u32 s36, s36, 0x40180
	s_addc_u32 s37, s37, 0
	s_add_u32 s72, s30, 0x200
	s_addc_u32 s73, s31, 0
	s_mov_b32 s74, 0
	.p2align	6

.LBB0_819:
	s_add_u32 s81, s30, 0x200
	s_addc_u32 s82, s31, 0
	s_add_i32 s55, 0, 0x14000
	s_add_i32 s52, 0, 0x10000
	v_add_u32_e32 v199, s55, v167
	v_add_u32_e32 v200, s52, v167
	ds_read_b128 v[10:13], v199
	ds_read_b128 v[14:17], v199 offset:1024
	ds_read_b128 v[2:5], v199 offset:2048
	ds_read_b128 v[6:9], v199 offset:3072
	ds_read_b128 v[22:25], v200 offset:3072
	ds_read_b128 v[18:21], v200 offset:2048
	ds_read_b128 v[30:33], v200 offset:1024
	ds_read_b128 v[26:29], v200
	s_lshl_b32 s14, s80, 10
	s_add_i32 s83, s14, 0
	s_add_i32 s83, s83, 0x20400
	v_mov_b32_e32 v191, v35
	v_mov_b32_e32 v175, v35
	s_add_i32 s84, s69, 0xc000
	v_readlane_b32 s26, v253, 28
	s_mov_b32 m0, s84
	v_readlane_b32 s27, v253, 29
	s_add_i32 s53, s69, 0xe000
	ds_read_b128 v[202:205], v169
	ds_read_b128 v[206:209], v169 offset:1024
	ds_read_b128 v[222:225], v169 offset:2048
	ds_read_b128 v[226:229], v169 offset:3072
	ds_read_b128 v[230:233], v169 offset:4096
	ds_read_b128 v[234:237], v169 offset:5120
	ds_read_b128 v[238:241], v169 offset:6144
	ds_read_b128 v[242:245], v169 offset:7168
	global_load_lds_dwordx4 v190, s[26:27]
	s_mov_b32 m0, s53
	s_nop 0
	global_load_lds_dwordx4 v174, s[26:27]
	s_waitcnt vmcnt(8)
	s_waitcnt lgkmcnt(0)
	s_barrier
	s_setprio 1
	s_waitcnt lgkmcnt(0)
	v_mfma_f32_16x16x128_f8f6f4 v[160:163], v[26:33], v[202:209], 0
	v_mfma_f32_16x16x128_f8f6f4 v[156:159], v[18:25], v[202:209], 0
	v_mfma_f32_16x16x128_f8f6f4 v[148:151], v[18:25], v[222:229], 0
	v_mfma_f32_16x16x128_f8f6f4 v[152:155], v[26:33], v[222:229], 0
	v_mfma_f32_16x16x128_f8f6f4 v[144:147], v[26:33], v[230:237], 0
	v_mfma_f32_16x16x128_f8f6f4 v[140:143], v[18:25], v[230:237], 0
	v_mfma_f32_16x16x128_f8f6f4 v[132:135], v[18:25], v[238:245], 0
	v_mfma_f32_16x16x128_f8f6f4 v[136:139], v[26:33], v[238:245], 0
	s_setprio 0
	s_setprio 1
	v_mfma_f32_16x16x128_f8f6f4 v[128:131], v[10:17], v[202:209], 0
	v_mfma_f32_16x16x128_f8f6f4 v[124:127], v[2:9], v[202:209], 0
	v_mfma_f32_16x16x128_f8f6f4 v[116:119], v[2:9], v[222:229], 0
	v_mfma_f32_16x16x128_f8f6f4 v[120:123], v[10:17], v[222:229], 0
	v_mfma_f32_16x16x128_f8f6f4 v[112:115], v[10:17], v[230:237], 0
	v_mfma_f32_16x16x128_f8f6f4 v[108:111], v[2:9], v[230:237], 0
	v_mfma_f32_16x16x128_f8f6f4 v[100:103], v[2:9], v[238:245], 0
	v_mfma_f32_16x16x128_f8f6f4 v[104:107], v[10:17], v[238:245], 0
	s_setprio 0
	s_barrier
	s_add_i32 s52, s52, s68
	v_lshl_add_u64 v[194:195], s[30:31], 0, v[170:171]
	s_add_i32 s85, s52, 0x2000
	v_lshl_add_u64 v[178:179], v[194:195], 0, s[28:29]
	s_mov_b32 m0, s52
	v_lshl_add_u64 v[196:197], s[30:31], 0, v[172:173]
	s_add_u32 s36, s30, 0x20100
	ds_read_b128 v[202:205], v169 offset:16384
	ds_read_b128 v[206:209], v169 offset:17408
	ds_read_b128 v[222:225], v169 offset:18432
	ds_read_b128 v[226:229], v169 offset:19456
	ds_read_b128 v[230:233], v169 offset:20480
	ds_read_b128 v[234:237], v169 offset:21504
	ds_read_b128 v[238:241], v169 offset:22528
	ds_read_b128 v[242:245], v169 offset:23552
	global_load_lds_dwordx4 v[178:179], off
	v_lshl_add_u64 v[178:179], v[196:197], 0, s[28:29]
	s_mov_b32 m0, s85
	s_addc_u32 s37, s31, 0
	s_add_i32 s55, s55, s68
	global_load_lds_dwordx4 v[178:179], off
	v_lshl_add_u64 v[178:179], s[36:37], 0, v[170:171]
	s_mov_b32 m0, s55
	s_add_i32 s65, s55, 0x2000
	global_load_lds_dwordx4 v[178:179], off
	v_lshl_add_u64 v[178:179], s[36:37], 0, v[172:173]
	s_mov_b32 m0, s65
	v_readlane_b32 s26, v253, 37
	global_load_lds_dwordx4 v[178:179], off
	s_mov_b32 m0, s69
	v_readlane_b32 s27, v253, 38
	s_nop 4
	global_load_lds_dwordx4 v34, s[26:27]
	s_mov_b32 m0, s70
	s_nop 0
	global_load_lds_dwordx4 v192, s[26:27]
	s_waitcnt vmcnt(8)
	s_waitcnt lgkmcnt(0)
	s_barrier
	s_setprio 1
	s_waitcnt lgkmcnt(0)
	v_mfma_f32_16x16x128_f8f6f4 v[96:99], v[26:33], v[202:209], 0
	v_mfma_f32_16x16x128_f8f6f4 v[92:95], v[18:25], v[202:209], 0
	v_mfma_f32_16x16x128_f8f6f4 v[84:87], v[18:25], v[222:229], 0
	v_mfma_f32_16x16x128_f8f6f4 v[88:91], v[26:33], v[222:229], 0
	v_mfma_f32_16x16x128_f8f6f4 v[80:83], v[26:33], v[230:237], 0
	v_mfma_f32_16x16x128_f8f6f4 v[76:79], v[18:25], v[230:237], 0
	v_mfma_f32_16x16x128_f8f6f4 v[68:71], v[18:25], v[238:245], 0
	v_mfma_f32_16x16x128_f8f6f4 v[72:75], v[26:33], v[238:245], 0
	s_setprio 0
	s_setprio 1
	v_mfma_f32_16x16x128_f8f6f4 v[64:67], v[10:17], v[202:209], 0
	v_mfma_f32_16x16x128_f8f6f4 v[60:63], v[2:9], v[202:209], 0
	v_mfma_f32_16x16x128_f8f6f4 v[52:55], v[2:9], v[222:229], 0
	v_mfma_f32_16x16x128_f8f6f4 v[56:59], v[10:17], v[222:229], 0
	v_mfma_f32_16x16x128_f8f6f4 v[48:51], v[10:17], v[230:237], 0
	v_mfma_f32_16x16x128_f8f6f4 v[44:47], v[2:9], v[230:237], 0
	v_mfma_f32_16x16x128_f8f6f4 v[36:39], v[2:9], v[238:245], 0
	v_mfma_f32_16x16x128_f8f6f4 v[40:43], v[10:17], v[238:245], 0
	s_setprio 0
	s_barrier
	s_add_i32 s54, 0, 0x18000
	s_add_i32 s51, 0, 0x1c000
	v_add_u32_e32 v201, s54, v167
	v_add_u32_e32 v202, s51, v167
	ds_read_b128 v[26:29], v201
	ds_read_b128 v[30:33], v201 offset:1024
	ds_read_b128 v[18:21], v201 offset:2048
	ds_read_b128 v[22:25], v201 offset:3072
	ds_read_b128 v[10:13], v202
	ds_read_b128 v[14:17], v202 offset:1024
	ds_read_b128 v[2:5], v202 offset:2048
	ds_read_b128 v[6:9], v202 offset:3072
	s_mov_b32 m0, s71
	ds_read_b128 v[204:207], v169 offset:32768
	ds_read_b128 v[208:211], v169 offset:33792
	ds_read_b128 v[222:225], v169 offset:34816
	ds_read_b128 v[226:229], v169 offset:35840
	ds_read_b128 v[230:233], v169 offset:36864
	ds_read_b128 v[234:237], v169 offset:37888
	ds_read_b128 v[238:241], v169 offset:38912
	ds_read_b128 v[242:245], v169 offset:39936
	global_load_lds_dwordx4 v189, s[26:27]
	s_mov_b32 m0, s72
	s_nop 0
	global_load_lds_dwordx4 v198, s[26:27]
	s_waitcnt vmcnt(8)
	s_waitcnt lgkmcnt(0)
	s_barrier
	s_setprio 1
	s_waitcnt lgkmcnt(0)
	v_mfma_f32_16x16x128_f8f6f4 v[160:163], v[26:33], v[204:211], v[160:163]
	v_mfma_f32_16x16x128_f8f6f4 v[156:159], v[18:25], v[204:211], v[156:159]
	v_mfma_f32_16x16x128_f8f6f4 v[148:151], v[18:25], v[222:229], v[148:151]
	v_mfma_f32_16x16x128_f8f6f4 v[152:155], v[26:33], v[222:229], v[152:155]
	v_mfma_f32_16x16x128_f8f6f4 v[144:147], v[26:33], v[230:237], v[144:147]
	v_mfma_f32_16x16x128_f8f6f4 v[140:143], v[18:25], v[230:237], v[140:143]
	v_mfma_f32_16x16x128_f8f6f4 v[132:135], v[18:25], v[238:245], v[132:135]
	v_mfma_f32_16x16x128_f8f6f4 v[136:139], v[26:33], v[238:245], v[136:139]
	s_setprio 0
	s_setprio 1
	v_mfma_f32_16x16x128_f8f6f4 v[128:131], v[10:17], v[204:211], v[128:131]
	v_mfma_f32_16x16x128_f8f6f4 v[124:127], v[2:9], v[204:211], v[124:127]
	v_mfma_f32_16x16x128_f8f6f4 v[116:119], v[2:9], v[222:229], v[116:119]
	v_mfma_f32_16x16x128_f8f6f4 v[120:123], v[10:17], v[222:229], v[120:123]
	v_mfma_f32_16x16x128_f8f6f4 v[112:115], v[10:17], v[230:237], v[112:115]
	v_mfma_f32_16x16x128_f8f6f4 v[108:111], v[2:9], v[230:237], v[108:111]
	v_mfma_f32_16x16x128_f8f6f4 v[100:103], v[2:9], v[238:245], v[100:103]
	v_mfma_f32_16x16x128_f8f6f4 v[104:107], v[10:17], v[238:245], v[104:107]
	s_setprio 0
	s_barrier
	s_add_i32 s54, s54, s68
	s_mov_b64 s[26:27], 0x180
	s_add_i32 s50, s54, 0x2000
	v_lshl_add_u64 v[178:179], v[194:195], 0, s[26:27]
	s_mov_b32 m0, s54
	s_add_u32 s30, s30, 0x20180
	ds_read_b128 v[204:207], v169 offset:49152
	ds_read_b128 v[208:211], v169 offset:50176
	ds_read_b128 v[222:225], v169 offset:51200
	ds_read_b128 v[226:229], v169 offset:52224
	ds_read_b128 v[230:233], v169 offset:53248
	ds_read_b128 v[234:237], v169 offset:54272
	ds_read_b128 v[238:241], v169 offset:55296
	ds_read_b128 v[242:245], v169 offset:56320
	global_load_lds_dwordx4 v[178:179], off
	v_lshl_add_u64 v[178:179], v[196:197], 0, s[26:27]
	s_mov_b32 m0, s50
	s_addc_u32 s31, s31, 0
	s_add_i32 s51, s51, s68
	global_load_lds_dwordx4 v[178:179], off
	v_lshl_add_u64 v[178:179], s[30:31], 0, v[170:171]
	s_mov_b32 m0, s51
	s_add_i32 s64, s51, 0x2000
	global_load_lds_dwordx4 v[178:179], off
	v_lshl_add_u64 v[178:179], s[30:31], 0, v[172:173]
	s_mov_b32 m0, s64
	v_readlane_b32 s26, v253, 39
	global_load_lds_dwordx4 v[178:179], off
	s_mov_b32 m0, s75
	v_readlane_b32 s27, v253, 40
	s_nop 4
	global_load_lds_dwordx4 v34, s[26:27]
	s_mov_b32 m0, s76
	s_nop 0
	global_load_lds_dwordx4 v192, s[26:27]
	s_waitcnt vmcnt(8)
	s_waitcnt lgkmcnt(0)
	s_barrier
	s_setprio 1
	s_waitcnt lgkmcnt(0)
	v_mfma_f32_16x16x128_f8f6f4 v[96:99], v[26:33], v[204:211], v[96:99]
	v_mfma_f32_16x16x128_f8f6f4 v[92:95], v[18:25], v[204:211], v[92:95]
	v_mfma_f32_16x16x128_f8f6f4 v[84:87], v[18:25], v[222:229], v[84:87]
	v_mfma_f32_16x16x128_f8f6f4 v[88:91], v[26:33], v[222:229], v[88:91]
	v_mfma_f32_16x16x128_f8f6f4 v[80:83], v[26:33], v[230:237], v[80:83]
	v_mfma_f32_16x16x128_f8f6f4 v[76:79], v[18:25], v[230:237], v[76:79]
	v_mfma_f32_16x16x128_f8f6f4 v[68:71], v[18:25], v[238:245], v[68:71]
	v_mfma_f32_16x16x128_f8f6f4 v[72:75], v[26:33], v[238:245], v[72:75]
	s_setprio 0
	s_setprio 1
	v_mfma_f32_16x16x128_f8f6f4 v[64:67], v[10:17], v[204:211], v[64:67]
	v_mfma_f32_16x16x128_f8f6f4 v[60:63], v[2:9], v[204:211], v[60:63]
	v_mfma_f32_16x16x128_f8f6f4 v[52:55], v[2:9], v[222:229], v[52:55]
	v_mfma_f32_16x16x128_f8f6f4 v[56:59], v[10:17], v[222:229], v[56:59]
	v_mfma_f32_16x16x128_f8f6f4 v[48:51], v[10:17], v[230:237], v[48:51]
	v_mfma_f32_16x16x128_f8f6f4 v[44:47], v[2:9], v[230:237], v[44:47]
	v_mfma_f32_16x16x128_f8f6f4 v[36:39], v[2:9], v[238:245], v[36:39]
	v_mfma_f32_16x16x128_f8f6f4 v[40:43], v[10:17], v[238:245], v[40:43]
	s_setprio 0
	s_barrier
	v_lshl_add_u64 v[18:19], s[26:27], 0, v[174:175]
	v_lshl_add_u64 v[20:21], s[26:27], 0, v[190:191]
	s_mov_b32 s63, 0
	s_mov_b64 s[30:31], 0
	s_branch .LBB0_821
	.p2align	6

.LBB0_899:
	s_mul_i32 s14, s81, 0xe0000
	s_add_u32 s40, s44, s14
	s_addc_u32 s41, s45, 0
	s_and_b64 s[6:7], s[6:7], exec
	s_cselect_b32 s52, s41, s43
	s_cselect_b32 s53, s40, s42
	s_add_i32 s54, 0, 0x10000
	s_add_i32 s65, 0, 0x14000
	v_add_u32_e32 v34, s54, v167
	v_add_u32_e32 v206, s65, v167
	ds_read_b128 v[26:29], v34
	ds_read_b128 v[30:33], v34 offset:1024
	ds_read_b128 v[18:21], v34 offset:2048
	ds_read_b128 v[22:25], v34 offset:3072
	ds_read_b128 v[10:13], v206
	ds_read_b128 v[14:17], v206 offset:1024
	ds_read_b128 v[2:5], v206 offset:2048
	ds_read_b128 v[6:9], v206 offset:3072
	s_add_u32 s6, s42, 0x70080
	s_addc_u32 s7, s43, 0
	s_add_i32 s84, s72, 0xc000
	v_lshl_add_u64 v[216:217], s[6:7], 0, v[174:175]
	s_mov_b32 m0, s84
	s_add_i32 s85, s72, 0xe000
	ds_read_b128 v[178:181], v189
	ds_read_b128 v[182:185], v189 offset:1024
	ds_read_b128 v[198:201], v189 offset:2048
	ds_read_b128 v[202:205], v189 offset:3072
	ds_read_b128 v[208:211], v189 offset:4096
	ds_read_b128 v[212:215], v189 offset:5120
	ds_read_b128 v[222:225], v189 offset:6144
	ds_read_b128 v[226:229], v189 offset:7168
	global_load_lds_dwordx4 v[216:217], off
	v_lshl_add_u64 v[216:217], s[6:7], 0, v[170:171]
	s_mov_b32 m0, s85
	s_nop 0
	global_load_lds_dwordx4 v[216:217], off
	s_waitcnt vmcnt(8)
	s_waitcnt lgkmcnt(0)
	s_barrier
	s_setprio 1
	s_waitcnt lgkmcnt(0)
	v_mfma_f32_16x16x128_f8f6f4 v[160:163], v[26:33], v[178:185], 0
	v_mfma_f32_16x16x128_f8f6f4 v[156:159], v[18:25], v[178:185], 0
	v_mfma_f32_16x16x128_f8f6f4 v[148:151], v[18:25], v[198:205], 0
	v_mfma_f32_16x16x128_f8f6f4 v[152:155], v[26:33], v[198:205], 0
	v_mfma_f32_16x16x128_f8f6f4 v[144:147], v[26:33], v[208:215], 0
	v_mfma_f32_16x16x128_f8f6f4 v[140:143], v[18:25], v[208:215], 0
	v_mfma_f32_16x16x128_f8f6f4 v[132:135], v[18:25], v[222:229], 0
	v_mfma_f32_16x16x128_f8f6f4 v[136:139], v[26:33], v[222:229], 0
	s_setprio 0
	s_setprio 1
	v_mfma_f32_16x16x128_f8f6f4 v[128:131], v[10:17], v[178:185], 0
	v_mfma_f32_16x16x128_f8f6f4 v[124:127], v[2:9], v[178:185], 0
	v_mfma_f32_16x16x128_f8f6f4 v[116:119], v[2:9], v[198:205], 0
	v_mfma_f32_16x16x128_f8f6f4 v[120:123], v[10:17], v[198:205], 0
	v_mfma_f32_16x16x128_f8f6f4 v[112:115], v[10:17], v[208:215], 0
	v_mfma_f32_16x16x128_f8f6f4 v[108:111], v[2:9], v[208:215], 0
	v_mfma_f32_16x16x128_f8f6f4 v[100:103], v[2:9], v[222:229], 0
	v_mfma_f32_16x16x128_f8f6f4 v[104:107], v[10:17], v[222:229], 0
	s_setprio 0
	s_barrier
	v_lshl_add_u64 v[198:199], v[196:197], 0, v[172:173]
	s_add_i32 s54, s54, s71
	v_lshl_add_u64 v[200:201], v[198:199], 0, s[28:29]
	s_mov_b32 m0, s54
	ds_read_b128 v[178:181], v189 offset:16384
	ds_read_b128 v[182:185], v189 offset:17408
	ds_read_b128 v[208:211], v189 offset:18432
	ds_read_b128 v[212:215], v189 offset:19456
	ds_read_b128 v[222:225], v189 offset:20480
	ds_read_b128 v[226:229], v189 offset:21504
	ds_read_b128 v[230:233], v189 offset:22528
	ds_read_b128 v[234:237], v189 offset:23552
	global_load_lds_dwordx4 v[200:201], off
	v_lshl_add_u64 v[200:201], v[196:197], 0, v[168:169]
	s_add_i32 s55, s54, 0x2000
	v_lshl_add_u64 v[202:203], v[200:201], 0, s[28:29]
	s_mov_b32 m0, s55
	s_mov_b64 s[6:7], 0x70100
	global_load_lds_dwordx4 v[202:203], off
	v_lshl_add_u64 v[202:203], v[196:197], 0, s[6:7]
	s_add_i32 s65, s65, s71
	v_lshl_add_u64 v[204:205], v[202:203], 0, v[172:173]
	s_mov_b32 m0, s65
	s_add_i32 s67, s65, 0x2000
	global_load_lds_dwordx4 v[204:205], off
	v_lshl_add_u64 v[202:203], v[202:203], 0, v[168:169]
	s_mov_b32 m0, s67
	s_nop 0
	global_load_lds_dwordx4 v[202:203], off
	v_lshl_add_u64 v[202:203], s[42:43], 0, v[174:175]
	v_lshl_add_u64 v[204:205], v[202:203], 0, s[28:29]
	s_mov_b32 m0, s72
	s_nop 0
	global_load_lds_dwordx4 v[204:205], off
	v_lshl_add_u64 v[204:205], s[42:43], 0, v[170:171]
	v_lshl_add_u64 v[216:217], v[204:205], 0, s[28:29]
	s_mov_b32 m0, s73
	s_nop 0
	global_load_lds_dwordx4 v[216:217], off
	s_waitcnt vmcnt(8)
	s_waitcnt lgkmcnt(0)
	s_barrier
	s_setprio 1
	s_waitcnt lgkmcnt(0)
	v_mfma_f32_16x16x128_f8f6f4 v[96:99], v[26:33], v[178:185], 0
	v_mfma_f32_16x16x128_f8f6f4 v[92:95], v[18:25], v[178:185], 0
	v_mfma_f32_16x16x128_f8f6f4 v[84:87], v[18:25], v[208:215], 0
	v_mfma_f32_16x16x128_f8f6f4 v[88:91], v[26:33], v[208:215], 0
	v_mfma_f32_16x16x128_f8f6f4 v[80:83], v[26:33], v[222:229], 0
	v_mfma_f32_16x16x128_f8f6f4 v[76:79], v[18:25], v[222:229], 0
	v_mfma_f32_16x16x128_f8f6f4 v[68:71], v[18:25], v[230:237], 0
	v_mfma_f32_16x16x128_f8f6f4 v[72:75], v[26:33], v[230:237], 0
	s_setprio 0
	s_setprio 1
	v_mfma_f32_16x16x128_f8f6f4 v[64:67], v[10:17], v[178:185], 0
	v_mfma_f32_16x16x128_f8f6f4 v[60:63], v[2:9], v[178:185], 0
	v_mfma_f32_16x16x128_f8f6f4 v[52:55], v[2:9], v[208:215], 0
	v_mfma_f32_16x16x128_f8f6f4 v[56:59], v[10:17], v[208:215], 0
	v_mfma_f32_16x16x128_f8f6f4 v[48:51], v[10:17], v[222:229], 0
	v_mfma_f32_16x16x128_f8f6f4 v[44:47], v[2:9], v[222:229], 0
	v_mfma_f32_16x16x128_f8f6f4 v[36:39], v[2:9], v[230:237], 0
	v_mfma_f32_16x16x128_f8f6f4 v[40:43], v[10:17], v[230:237], 0
	s_setprio 0
	s_barrier
	s_add_i32 s50, 0, 0x18000
	s_add_i32 s63, 0, 0x1c000
	v_add_u32_e32 v207, s50, v167
	v_add_u32_e32 v208, s63, v167
	ds_read_b128 v[26:29], v207
	ds_read_b128 v[30:33], v207 offset:1024
	ds_read_b128 v[18:21], v207 offset:2048
	ds_read_b128 v[22:25], v207 offset:3072
	ds_read_b128 v[10:13], v208
	ds_read_b128 v[14:17], v208 offset:1024
	ds_read_b128 v[2:5], v208 offset:2048
	ds_read_b128 v[6:9], v208 offset:3072
	s_add_u32 s6, s42, 0x70100
	s_addc_u32 s7, s43, 0
	s_mov_b32 m0, s74
	v_lshl_add_u64 v[218:219], s[6:7], 0, v[174:175]
	ds_read_b128 v[178:181], v189 offset:32768
	ds_read_b128 v[182:185], v189 offset:33792
	ds_read_b128 v[210:213], v189 offset:34816
	ds_read_b128 v[214:217], v189 offset:35840
	ds_read_b128 v[222:225], v189 offset:36864
	ds_read_b128 v[226:229], v189 offset:37888
	ds_read_b128 v[230:233], v189 offset:38912
	ds_read_b128 v[234:237], v189 offset:39936
	global_load_lds_dwordx4 v[218:219], off
	v_lshl_add_u64 v[218:219], s[6:7], 0, v[170:171]
	s_mov_b32 m0, s75
	s_nop 0
	global_load_lds_dwordx4 v[218:219], off
	s_waitcnt vmcnt(8)
	s_waitcnt lgkmcnt(0)
	s_barrier
	s_setprio 1
	s_waitcnt lgkmcnt(0)
	v_mfma_f32_16x16x128_f8f6f4 v[160:163], v[26:33], v[178:185], v[160:163]
	v_mfma_f32_16x16x128_f8f6f4 v[156:159], v[18:25], v[178:185], v[156:159]
	v_mfma_f32_16x16x128_f8f6f4 v[148:151], v[18:25], v[210:217], v[148:151]
	v_mfma_f32_16x16x128_f8f6f4 v[152:155], v[26:33], v[210:217], v[152:155]
	v_mfma_f32_16x16x128_f8f6f4 v[144:147], v[26:33], v[222:229], v[144:147]
	v_mfma_f32_16x16x128_f8f6f4 v[140:143], v[18:25], v[222:229], v[140:143]
	v_mfma_f32_16x16x128_f8f6f4 v[132:135], v[18:25], v[230:237], v[132:135]
	v_mfma_f32_16x16x128_f8f6f4 v[136:139], v[26:33], v[230:237], v[136:139]
	s_setprio 0
	s_setprio 1
	v_mfma_f32_16x16x128_f8f6f4 v[128:131], v[10:17], v[178:185], v[128:131]
	v_mfma_f32_16x16x128_f8f6f4 v[124:127], v[2:9], v[178:185], v[124:127]
	v_mfma_f32_16x16x128_f8f6f4 v[116:119], v[2:9], v[210:217], v[116:119]
	v_mfma_f32_16x16x128_f8f6f4 v[120:123], v[10:17], v[210:217], v[120:123]
	v_mfma_f32_16x16x128_f8f6f4 v[112:115], v[10:17], v[222:229], v[112:115]
	v_mfma_f32_16x16x128_f8f6f4 v[108:111], v[2:9], v[222:229], v[108:111]
	v_mfma_f32_16x16x128_f8f6f4 v[100:103], v[2:9], v[230:237], v[100:103]
	v_mfma_f32_16x16x128_f8f6f4 v[104:107], v[10:17], v[230:237], v[104:107]
	s_setprio 0
	s_barrier
	s_mov_b64 s[6:7], 0x180
	s_add_i32 s50, s50, s71
	v_lshl_add_u64 v[198:199], v[198:199], 0, s[6:7]
	s_mov_b32 m0, s50
	s_add_i32 s51, s50, 0x2000
	ds_read_b128 v[178:181], v189 offset:49152
	ds_read_b128 v[182:185], v189 offset:50176
	ds_read_b128 v[210:213], v189 offset:51200
	ds_read_b128 v[214:217], v189 offset:52224
	ds_read_b128 v[222:225], v189 offset:53248
	ds_read_b128 v[226:229], v189 offset:54272
	ds_read_b128 v[230:233], v189 offset:55296
	ds_read_b128 v[234:237], v189 offset:56320
	global_load_lds_dwordx4 v[198:199], off
	v_lshl_add_u64 v[198:199], v[200:201], 0, s[6:7]
	s_mov_b32 m0, s51
	s_add_i32 s63, s63, s71
	global_load_lds_dwordx4 v[198:199], off
	v_lshl_add_u64 v[198:199], v[196:197], 0, s[26:27]
	v_lshl_add_u64 v[200:201], v[198:199], 0, v[172:173]
	s_mov_b32 m0, s63
	s_add_i32 s64, s63, 0x2000
	global_load_lds_dwordx4 v[200:201], off
	v_lshl_add_u64 v[198:199], v[198:199], 0, v[168:169]
	s_mov_b32 m0, s64
	s_nop 0
	global_load_lds_dwordx4 v[198:199], off
	v_lshl_add_u64 v[198:199], v[202:203], 0, s[6:7]
	s_mov_b32 m0, s77
	s_nop 0
	global_load_lds_dwordx4 v[198:199], off
	v_lshl_add_u64 v[198:199], v[204:205], 0, s[6:7]
	s_mov_b32 m0, s78
	s_nop 0
	global_load_lds_dwordx4 v[198:199], off
	s_waitcnt vmcnt(8)
	s_waitcnt lgkmcnt(0)
	s_barrier
	s_setprio 1
	s_waitcnt lgkmcnt(0)
	v_mfma_f32_16x16x128_f8f6f4 v[96:99], v[26:33], v[178:185], v[96:99]
	v_mfma_f32_16x16x128_f8f6f4 v[92:95], v[18:25], v[178:185], v[92:95]
	v_mfma_f32_16x16x128_f8f6f4 v[84:87], v[18:25], v[210:217], v[84:87]
	v_mfma_f32_16x16x128_f8f6f4 v[88:91], v[26:33], v[210:217], v[88:91]
	v_mfma_f32_16x16x128_f8f6f4 v[80:83], v[26:33], v[222:229], v[80:83]
	v_mfma_f32_16x16x128_f8f6f4 v[76:79], v[18:25], v[222:229], v[76:79]
	v_mfma_f32_16x16x128_f8f6f4 v[68:71], v[18:25], v[230:237], v[68:71]
	v_mfma_f32_16x16x128_f8f6f4 v[72:75], v[26:33], v[230:237], v[72:75]
	s_setprio 0
	s_setprio 1
	v_mfma_f32_16x16x128_f8f6f4 v[64:67], v[10:17], v[178:185], v[64:67]
	v_mfma_f32_16x16x128_f8f6f4 v[60:63], v[2:9], v[178:185], v[60:63]
	v_mfma_f32_16x16x128_f8f6f4 v[52:55], v[2:9], v[210:217], v[52:55]
	v_mfma_f32_16x16x128_f8f6f4 v[56:59], v[10:17], v[210:217], v[56:59]
	v_mfma_f32_16x16x128_f8f6f4 v[48:51], v[10:17], v[222:229], v[48:51]
	v_mfma_f32_16x16x128_f8f6f4 v[44:47], v[2:9], v[222:229], v[44:47]
	v_mfma_f32_16x16x128_f8f6f4 v[36:39], v[2:9], v[230:237], v[36:39]
	v_mfma_f32_16x16x128_f8f6f4 v[40:43], v[10:17], v[230:237], v[40:43]
	s_setprio 0
	s_barrier
	s_mov_b64 s[6:7], 0x200
	v_lshl_add_u64 v[18:19], v[196:197], 0, s[6:7]
	s_mov_b32 s86, 0
	.p2align	6

.LBB0_953:
	s_add_u32 s95, s30, 0x200
	s_addc_u32 s96, s31, 0
	s_add_i32 s65, 0, 0x14000
	s_add_i32 s67, 0, 0x10000
	v_add_u32_e32 v199, s65, v167
	v_add_u32_e32 v200, s67, v167
	ds_read_b128 v[10:13], v199
	ds_read_b128 v[14:17], v199 offset:1024
	ds_read_b128 v[2:5], v199 offset:2048
	ds_read_b128 v[6:9], v199 offset:3072
	ds_read_b128 v[22:25], v200 offset:3072
	ds_read_b128 v[18:21], v200 offset:2048
	ds_read_b128 v[30:33], v200 offset:1024
	ds_read_b128 v[26:29], v200
	s_lshl_b32 s14, s94, 10
	s_add_i32 s97, s14, 0
	s_add_i32 s97, s97, 0x20400
	v_mov_b32_e32 v191, v35
	v_mov_b32_e32 v175, v35
	s_add_i32 s83, s52, 0xc000
	v_readlane_b32 s26, v253, 28
	s_mov_b32 m0, s83
	v_readlane_b32 s27, v253, 29
	s_add_i32 s53, s52, 0xe000
	ds_read_b128 v[178:181], v169
	ds_read_b128 v[182:185], v169 offset:1024
	ds_read_b128 v[202:205], v169 offset:2048
	ds_read_b128 v[206:209], v169 offset:3072
	ds_read_b128 v[210:213], v169 offset:4096
	ds_read_b128 v[214:217], v169 offset:5120
	ds_read_b128 v[222:225], v169 offset:6144
	ds_read_b128 v[226:229], v169 offset:7168
	global_load_lds_dwordx4 v190, s[26:27]
	s_mov_b32 m0, s53
	s_nop 0
	global_load_lds_dwordx4 v174, s[26:27]
	s_waitcnt vmcnt(8)
	s_waitcnt lgkmcnt(0)
	s_barrier
	s_setprio 1
	s_waitcnt lgkmcnt(0)
	v_mfma_f32_16x16x128_f8f6f4 v[160:163], v[26:33], v[178:185], 0
	v_mfma_f32_16x16x128_f8f6f4 v[156:159], v[18:25], v[178:185], 0
	v_mfma_f32_16x16x128_f8f6f4 v[148:151], v[18:25], v[202:209], 0
	v_mfma_f32_16x16x128_f8f6f4 v[152:155], v[26:33], v[202:209], 0
	v_mfma_f32_16x16x128_f8f6f4 v[144:147], v[26:33], v[210:217], 0
	v_mfma_f32_16x16x128_f8f6f4 v[140:143], v[18:25], v[210:217], 0
	v_mfma_f32_16x16x128_f8f6f4 v[132:135], v[18:25], v[222:229], 0
	v_mfma_f32_16x16x128_f8f6f4 v[136:139], v[26:33], v[222:229], 0
	s_setprio 0
	s_setprio 1
	v_mfma_f32_16x16x128_f8f6f4 v[128:131], v[10:17], v[178:185], 0
	v_mfma_f32_16x16x128_f8f6f4 v[124:127], v[2:9], v[178:185], 0
	v_mfma_f32_16x16x128_f8f6f4 v[116:119], v[2:9], v[202:209], 0
	v_mfma_f32_16x16x128_f8f6f4 v[120:123], v[10:17], v[202:209], 0
	v_mfma_f32_16x16x128_f8f6f4 v[112:115], v[10:17], v[210:217], 0
	v_mfma_f32_16x16x128_f8f6f4 v[108:111], v[2:9], v[210:217], 0
	v_mfma_f32_16x16x128_f8f6f4 v[100:103], v[2:9], v[222:229], 0
	v_mfma_f32_16x16x128_f8f6f4 v[104:107], v[10:17], v[222:229], 0
	s_setprio 0
	s_barrier
	v_lshl_add_u64 v[194:195], s[30:31], 0, v[170:171]
	s_add_i32 s67, s67, s82
	v_lshl_add_u64 v[196:197], v[194:195], 0, s[28:29]
	s_mov_b32 m0, s67
	s_add_i32 s55, s67, 0x2000
	ds_read_b128 v[178:181], v169 offset:16384
	ds_read_b128 v[182:185], v169 offset:17408
	ds_read_b128 v[202:205], v169 offset:18432
	ds_read_b128 v[206:209], v169 offset:19456
	ds_read_b128 v[210:213], v169 offset:20480
	ds_read_b128 v[214:217], v169 offset:21504
	ds_read_b128 v[222:225], v169 offset:22528
	ds_read_b128 v[226:229], v169 offset:23552
	global_load_lds_dwordx4 v[196:197], off
	v_lshl_add_u64 v[196:197], s[30:31], 0, v[172:173]
	s_add_u32 s46, s30, 0x20100
	v_lshl_add_u64 v[218:219], v[196:197], 0, s[28:29]
	s_mov_b32 m0, s55
	s_addc_u32 s47, s31, 0
	s_add_i32 s65, s65, s82
	global_load_lds_dwordx4 v[218:219], off
	v_lshl_add_u64 v[218:219], s[46:47], 0, v[170:171]
	s_mov_b32 m0, s65
	s_add_i32 s54, s65, 0x2000
	global_load_lds_dwordx4 v[218:219], off
	v_lshl_add_u64 v[218:219], s[46:47], 0, v[172:173]
	s_mov_b32 m0, s54
	v_readlane_b32 s26, v253, 37
	global_load_lds_dwordx4 v[218:219], off
	s_mov_b32 m0, s52
	v_readlane_b32 s27, v253, 38
	s_nop 4
	global_load_lds_dwordx4 v34, s[26:27]
	s_mov_b32 m0, s84
	s_nop 0
	global_load_lds_dwordx4 v192, s[26:27]
	s_waitcnt vmcnt(8)
	s_waitcnt lgkmcnt(0)
	s_barrier
	s_setprio 1
	s_waitcnt lgkmcnt(0)
	v_mfma_f32_16x16x128_f8f6f4 v[96:99], v[26:33], v[178:185], 0
	v_mfma_f32_16x16x128_f8f6f4 v[92:95], v[18:25], v[178:185], 0
	v_mfma_f32_16x16x128_f8f6f4 v[84:87], v[18:25], v[202:209], 0
	v_mfma_f32_16x16x128_f8f6f4 v[88:91], v[26:33], v[202:209], 0
	v_mfma_f32_16x16x128_f8f6f4 v[80:83], v[26:33], v[210:217], 0
	v_mfma_f32_16x16x128_f8f6f4 v[76:79], v[18:25], v[210:217], 0
	v_mfma_f32_16x16x128_f8f6f4 v[68:71], v[18:25], v[222:229], 0
	v_mfma_f32_16x16x128_f8f6f4 v[72:75], v[26:33], v[222:229], 0
	s_setprio 0
	s_setprio 1
	v_mfma_f32_16x16x128_f8f6f4 v[64:67], v[10:17], v[178:185], 0
	v_mfma_f32_16x16x128_f8f6f4 v[60:63], v[2:9], v[178:185], 0
	v_mfma_f32_16x16x128_f8f6f4 v[52:55], v[2:9], v[202:209], 0
	v_mfma_f32_16x16x128_f8f6f4 v[56:59], v[10:17], v[202:209], 0
	v_mfma_f32_16x16x128_f8f6f4 v[48:51], v[10:17], v[210:217], 0
	v_mfma_f32_16x16x128_f8f6f4 v[44:47], v[2:9], v[210:217], 0
	v_mfma_f32_16x16x128_f8f6f4 v[36:39], v[2:9], v[222:229], 0
	v_mfma_f32_16x16x128_f8f6f4 v[40:43], v[10:17], v[222:229], 0
	s_setprio 0
	s_barrier
	s_add_i32 s50, 0, 0x18000
	s_add_i32 s64, 0, 0x1c000
	v_add_u32_e32 v201, s50, v167
	v_add_u32_e32 v202, s64, v167
	ds_read_b128 v[26:29], v201
	ds_read_b128 v[30:33], v201 offset:1024
	ds_read_b128 v[18:21], v201 offset:2048
	ds_read_b128 v[22:25], v201 offset:3072
	ds_read_b128 v[10:13], v202
	ds_read_b128 v[14:17], v202 offset:1024
	ds_read_b128 v[2:5], v202 offset:2048
	ds_read_b128 v[6:9], v202 offset:3072
	s_mov_b32 m0, s85
	ds_read_b128 v[178:181], v169 offset:32768
	ds_read_b128 v[182:185], v169 offset:33792
	ds_read_b128 v[204:207], v169 offset:34816
	ds_read_b128 v[208:211], v169 offset:35840
	ds_read_b128 v[212:215], v169 offset:36864
	ds_read_b128 v[216:219], v169 offset:37888
	ds_read_b128 v[222:225], v169 offset:38912
	ds_read_b128 v[226:229], v169 offset:39936
	global_load_lds_dwordx4 v189, s[26:27]
	s_mov_b32 m0, s86
	s_nop 0
	global_load_lds_dwordx4 v198, s[26:27]
	s_waitcnt vmcnt(8)
	s_waitcnt lgkmcnt(0)
	s_barrier
	s_setprio 1
	s_waitcnt lgkmcnt(0)
	v_mfma_f32_16x16x128_f8f6f4 v[160:163], v[26:33], v[178:185], v[160:163]
	v_mfma_f32_16x16x128_f8f6f4 v[156:159], v[18:25], v[178:185], v[156:159]
	v_mfma_f32_16x16x128_f8f6f4 v[148:151], v[18:25], v[204:211], v[148:151]
	v_mfma_f32_16x16x128_f8f6f4 v[152:155], v[26:33], v[204:211], v[152:155]
	v_mfma_f32_16x16x128_f8f6f4 v[144:147], v[26:33], v[212:219], v[144:147]
	v_mfma_f32_16x16x128_f8f6f4 v[140:143], v[18:25], v[212:219], v[140:143]
	v_mfma_f32_16x16x128_f8f6f4 v[132:135], v[18:25], v[222:229], v[132:135]
	v_mfma_f32_16x16x128_f8f6f4 v[136:139], v[26:33], v[222:229], v[136:139]
	s_setprio 0
	s_setprio 1
	v_mfma_f32_16x16x128_f8f6f4 v[128:131], v[10:17], v[178:185], v[128:131]
	v_mfma_f32_16x16x128_f8f6f4 v[124:127], v[2:9], v[178:185], v[124:127]
	v_mfma_f32_16x16x128_f8f6f4 v[116:119], v[2:9], v[204:211], v[116:119]
	v_mfma_f32_16x16x128_f8f6f4 v[120:123], v[10:17], v[204:211], v[120:123]
	v_mfma_f32_16x16x128_f8f6f4 v[112:115], v[10:17], v[212:219], v[112:115]
	v_mfma_f32_16x16x128_f8f6f4 v[108:111], v[2:9], v[212:219], v[108:111]
	v_mfma_f32_16x16x128_f8f6f4 v[100:103], v[2:9], v[222:229], v[100:103]
	v_mfma_f32_16x16x128_f8f6f4 v[104:107], v[10:17], v[222:229], v[104:107]
	s_setprio 0
	s_barrier
	s_add_i32 s50, s50, s82
	s_mov_b64 s[26:27], 0x180
	s_add_i32 s51, s50, 0x2000
	v_lshl_add_u64 v[194:195], v[194:195], 0, s[26:27]
	s_mov_b32 m0, s50
	s_add_u32 s30, s30, 0x20180
	ds_read_b128 v[178:181], v169 offset:49152
	ds_read_b128 v[182:185], v169 offset:50176
	ds_read_b128 v[204:207], v169 offset:51200
	ds_read_b128 v[208:211], v169 offset:52224
	ds_read_b128 v[212:215], v169 offset:53248
	ds_read_b128 v[216:219], v169 offset:54272
	ds_read_b128 v[222:225], v169 offset:55296
	ds_read_b128 v[226:229], v169 offset:56320
	global_load_lds_dwordx4 v[194:195], off
	v_lshl_add_u64 v[194:195], v[196:197], 0, s[26:27]
	s_mov_b32 m0, s51
	s_addc_u32 s31, s31, 0
	s_add_i32 s64, s64, s82
	global_load_lds_dwordx4 v[194:195], off
	v_lshl_add_u64 v[194:195], s[30:31], 0, v[170:171]
	s_mov_b32 m0, s64
	s_add_i32 s63, s64, 0x2000
	global_load_lds_dwordx4 v[194:195], off
	v_lshl_add_u64 v[194:195], s[30:31], 0, v[172:173]
	s_mov_b32 m0, s63
	v_readlane_b32 s26, v253, 39
	global_load_lds_dwordx4 v[194:195], off
	s_mov_b32 m0, s90
	v_readlane_b32 s27, v253, 40
	s_nop 4
	global_load_lds_dwordx4 v34, s[26:27]
	s_mov_b32 m0, s91
	s_nop 0
	global_load_lds_dwordx4 v192, s[26:27]
	s_waitcnt vmcnt(8)
	s_waitcnt lgkmcnt(0)
	s_barrier
	s_setprio 1
	s_waitcnt lgkmcnt(0)
	v_mfma_f32_16x16x128_f8f6f4 v[96:99], v[26:33], v[178:185], v[96:99]
	v_mfma_f32_16x16x128_f8f6f4 v[92:95], v[18:25], v[178:185], v[92:95]
	v_mfma_f32_16x16x128_f8f6f4 v[84:87], v[18:25], v[204:211], v[84:87]
	v_mfma_f32_16x16x128_f8f6f4 v[88:91], v[26:33], v[204:211], v[88:91]
	v_mfma_f32_16x16x128_f8f6f4 v[80:83], v[26:33], v[212:219], v[80:83]
	v_mfma_f32_16x16x128_f8f6f4 v[76:79], v[18:25], v[212:219], v[76:79]
	v_mfma_f32_16x16x128_f8f6f4 v[68:71], v[18:25], v[222:229], v[68:71]
	v_mfma_f32_16x16x128_f8f6f4 v[72:75], v[26:33], v[222:229], v[72:75]
	s_setprio 0
	s_setprio 1
	v_mfma_f32_16x16x128_f8f6f4 v[64:67], v[10:17], v[178:185], v[64:67]
	v_mfma_f32_16x16x128_f8f6f4 v[60:63], v[2:9], v[178:185], v[60:63]
	v_mfma_f32_16x16x128_f8f6f4 v[52:55], v[2:9], v[204:211], v[52:55]
	v_mfma_f32_16x16x128_f8f6f4 v[56:59], v[10:17], v[204:211], v[56:59]
	v_mfma_f32_16x16x128_f8f6f4 v[48:51], v[10:17], v[212:219], v[48:51]
	v_mfma_f32_16x16x128_f8f6f4 v[44:47], v[2:9], v[212:219], v[44:47]
	v_mfma_f32_16x16x128_f8f6f4 v[36:39], v[2:9], v[222:229], v[36:39]
	v_mfma_f32_16x16x128_f8f6f4 v[40:43], v[10:17], v[222:229], v[40:43]
	s_setprio 0
	s_barrier
	v_lshl_add_u64 v[18:19], s[26:27], 0, v[174:175]
	v_lshl_add_u64 v[20:21], s[26:27], 0, v[190:191]
	s_mov_b32 s75, 0
	s_mov_b64 s[30:31], 0
	s_branch .LBB0_955
	.p2align	6

.LBB0_1086:
	s_lshl_b32 s10, s51, 18
	s_add_u32 s10, s20, s10
	s_addc_u32 s11, s21, 0
	s_and_b64 s[16:17], s[4:5], exec
	s_cselect_b32 s54, s11, s31
	s_cselect_b32 s55, s10, s30
	s_lshl_b32 s14, s50, 18
	s_add_u32 s16, s15, s14
	s_addc_u32 s17, s26, 0
	s_and_b64 s[36:37], s[4:5], exec
	s_cselect_b32 s56, s17, s23
	s_cselect_b32 s57, s16, s22
	s_add_i32 s60, 0, 0x10000
	s_add_i32 s62, 0, 0x14000
	v_add_u32_e32 v198, s60, v196
	v_add_u32_e32 v199, s62, v196
	ds_read_b128 v[26:29], v198
	ds_read_b128 v[30:33], v198 offset:1024
	ds_read_b128 v[18:21], v198 offset:2048
	ds_read_b128 v[22:25], v198 offset:3072
	ds_read_b128 v[10:13], v199
	ds_read_b128 v[14:17], v199 offset:1024
	ds_read_b128 v[2:5], v199 offset:2048
	ds_read_b128 v[6:9], v199 offset:3072
	s_add_u32 s36, s30, 0x20080
	s_addc_u32 s37, s31, 0
	s_add_i32 s58, s41, 0xc000
	v_lshl_add_u64 v[174:175], s[36:37], 0, v[168:169]
	s_mov_b32 m0, s58
	s_add_i32 s59, s41, 0xe000
	ds_read_b128 v[200:203], v197
	ds_read_b128 v[204:207], v197 offset:1024
	ds_read_b128 v[222:225], v197 offset:2048
	ds_read_b128 v[226:229], v197 offset:3072
	ds_read_b128 v[230:233], v197 offset:4096
	ds_read_b128 v[234:237], v197 offset:5120
	ds_read_b128 v[238:241], v197 offset:6144
	ds_read_b128 v[242:245], v197 offset:7168
	global_load_lds_dwordx4 v[174:175], off
	v_lshl_add_u64 v[174:175], s[36:37], 0, v[166:167]
	s_mov_b32 m0, s59
	s_nop 0
	global_load_lds_dwordx4 v[174:175], off
	s_waitcnt vmcnt(8)
	s_waitcnt lgkmcnt(0)
	s_barrier
	s_setprio 1
	s_waitcnt lgkmcnt(0)
	v_mfma_f32_16x16x128_f8f6f4 v[160:163], v[26:33], v[200:207], 0
	v_mfma_f32_16x16x128_f8f6f4 v[156:159], v[18:25], v[200:207], 0
	v_mfma_f32_16x16x128_f8f6f4 v[148:151], v[18:25], v[222:229], 0
	v_mfma_f32_16x16x128_f8f6f4 v[152:155], v[26:33], v[222:229], 0
	v_mfma_f32_16x16x128_f8f6f4 v[144:147], v[26:33], v[230:237], 0
	v_mfma_f32_16x16x128_f8f6f4 v[140:143], v[18:25], v[230:237], 0
	v_mfma_f32_16x16x128_f8f6f4 v[132:135], v[18:25], v[238:245], 0
	v_mfma_f32_16x16x128_f8f6f4 v[136:139], v[26:33], v[238:245], 0
	s_setprio 0
	s_setprio 1
	v_mfma_f32_16x16x128_f8f6f4 v[128:131], v[10:17], v[200:207], 0
	v_mfma_f32_16x16x128_f8f6f4 v[124:127], v[2:9], v[200:207], 0
	v_mfma_f32_16x16x128_f8f6f4 v[116:119], v[2:9], v[222:229], 0
	v_mfma_f32_16x16x128_f8f6f4 v[120:123], v[10:17], v[222:229], 0
	v_mfma_f32_16x16x128_f8f6f4 v[112:115], v[10:17], v[230:237], 0
	v_mfma_f32_16x16x128_f8f6f4 v[108:111], v[2:9], v[230:237], 0
	v_mfma_f32_16x16x128_f8f6f4 v[100:103], v[2:9], v[238:245], 0
	v_mfma_f32_16x16x128_f8f6f4 v[104:107], v[10:17], v[238:245], 0
	s_setprio 0
	s_barrier
	s_add_i32 s60, s60, s40
	v_lshl_add_u64 v[174:175], s[22:23], 0, v[34:35]
	s_add_i32 s61, s60, 0x2000
	v_lshl_add_u64 v[178:179], v[174:175], 0, s[28:29]
	s_mov_b32 m0, s60
	v_lshl_add_u64 v[190:191], s[22:23], 0, v[164:165]
	s_add_u32 s36, s22, 0x20100
	ds_read_b128 v[200:203], v197 offset:16384
	ds_read_b128 v[204:207], v197 offset:17408
	ds_read_b128 v[222:225], v197 offset:18432
	ds_read_b128 v[226:229], v197 offset:19456
	ds_read_b128 v[230:233], v197 offset:20480
	ds_read_b128 v[234:237], v197 offset:21504
	ds_read_b128 v[238:241], v197 offset:22528
	ds_read_b128 v[242:245], v197 offset:23552
	global_load_lds_dwordx4 v[178:179], off
	v_lshl_add_u64 v[178:179], v[190:191], 0, s[28:29]
	s_mov_b32 m0, s61
	s_addc_u32 s37, s23, 0
	s_add_i32 s62, s62, s40
	global_load_lds_dwordx4 v[178:179], off
	v_lshl_add_u64 v[178:179], s[36:37], 0, v[34:35]
	s_mov_b32 m0, s62
	s_add_i32 s63, s62, 0x2000
	global_load_lds_dwordx4 v[178:179], off
	v_lshl_add_u64 v[178:179], s[36:37], 0, v[164:165]
	s_mov_b32 m0, s63
	v_lshl_add_u64 v[192:193], s[30:31], 0, v[168:169]
	global_load_lds_dwordx4 v[178:179], off
	v_lshl_add_u64 v[178:179], v[192:193], 0, s[28:29]
	s_mov_b32 m0, s41
	v_lshl_add_u64 v[194:195], s[30:31], 0, v[166:167]
	global_load_lds_dwordx4 v[178:179], off
	v_lshl_add_u64 v[178:179], v[194:195], 0, s[28:29]
	s_mov_b32 m0, s42
	s_nop 0
	global_load_lds_dwordx4 v[178:179], off
	s_waitcnt vmcnt(8)
	s_waitcnt lgkmcnt(0)
	s_barrier
	s_setprio 1
	s_waitcnt lgkmcnt(0)
	v_mfma_f32_16x16x128_f8f6f4 v[96:99], v[26:33], v[200:207], 0
	v_mfma_f32_16x16x128_f8f6f4 v[92:95], v[18:25], v[200:207], 0
	v_mfma_f32_16x16x128_f8f6f4 v[84:87], v[18:25], v[222:229], 0
	v_mfma_f32_16x16x128_f8f6f4 v[88:91], v[26:33], v[222:229], 0
	v_mfma_f32_16x16x128_f8f6f4 v[80:83], v[26:33], v[230:237], 0
	v_mfma_f32_16x16x128_f8f6f4 v[76:79], v[18:25], v[230:237], 0
	v_mfma_f32_16x16x128_f8f6f4 v[68:71], v[18:25], v[238:245], 0
	v_mfma_f32_16x16x128_f8f6f4 v[72:75], v[26:33], v[238:245], 0
	s_setprio 0
	s_setprio 1
	v_mfma_f32_16x16x128_f8f6f4 v[64:67], v[10:17], v[200:207], 0
	v_mfma_f32_16x16x128_f8f6f4 v[60:63], v[2:9], v[200:207], 0
	v_mfma_f32_16x16x128_f8f6f4 v[52:55], v[2:9], v[222:229], 0
	v_mfma_f32_16x16x128_f8f6f4 v[56:59], v[10:17], v[222:229], 0
	v_mfma_f32_16x16x128_f8f6f4 v[48:51], v[10:17], v[230:237], 0
	v_mfma_f32_16x16x128_f8f6f4 v[44:47], v[2:9], v[230:237], 0
	v_mfma_f32_16x16x128_f8f6f4 v[36:39], v[2:9], v[238:245], 0
	v_mfma_f32_16x16x128_f8f6f4 v[40:43], v[10:17], v[238:245], 0
	s_setprio 0
	s_barrier
	s_add_i32 s64, 0, 0x18000
	s_add_i32 s66, 0, 0x1c000
	v_add_u32_e32 v200, s64, v196
	v_add_u32_e32 v201, s66, v196
	ds_read_b128 v[26:29], v200
	ds_read_b128 v[30:33], v200 offset:1024
	ds_read_b128 v[18:21], v200 offset:2048
	ds_read_b128 v[22:25], v200 offset:3072
	ds_read_b128 v[10:13], v201
	ds_read_b128 v[14:17], v201 offset:1024
	ds_read_b128 v[2:5], v201 offset:2048
	ds_read_b128 v[6:9], v201 offset:3072
	s_add_u32 s36, s30, 0x20100
	s_addc_u32 s37, s31, 0
	s_mov_b32 m0, s43
	v_lshl_add_u64 v[178:179], s[36:37], 0, v[168:169]
	ds_read_b128 v[202:205], v197 offset:32768
	ds_read_b128 v[206:209], v197 offset:33792
	ds_read_b128 v[222:225], v197 offset:34816
	ds_read_b128 v[226:229], v197 offset:35840
	ds_read_b128 v[230:233], v197 offset:36864
	ds_read_b128 v[234:237], v197 offset:37888
	ds_read_b128 v[238:241], v197 offset:38912
	ds_read_b128 v[242:245], v197 offset:39936
	global_load_lds_dwordx4 v[178:179], off
	v_lshl_add_u64 v[178:179], s[36:37], 0, v[166:167]
	s_mov_b32 m0, s44
	s_nop 0
	global_load_lds_dwordx4 v[178:179], off
	s_waitcnt vmcnt(8)
	s_waitcnt lgkmcnt(0)
	s_barrier
	s_setprio 1
	s_waitcnt lgkmcnt(0)
	v_mfma_f32_16x16x128_f8f6f4 v[160:163], v[26:33], v[202:209], v[160:163]
	v_mfma_f32_16x16x128_f8f6f4 v[156:159], v[18:25], v[202:209], v[156:159]
	v_mfma_f32_16x16x128_f8f6f4 v[148:151], v[18:25], v[222:229], v[148:151]
	v_mfma_f32_16x16x128_f8f6f4 v[152:155], v[26:33], v[222:229], v[152:155]
	v_mfma_f32_16x16x128_f8f6f4 v[144:147], v[26:33], v[230:237], v[144:147]
	v_mfma_f32_16x16x128_f8f6f4 v[140:143], v[18:25], v[230:237], v[140:143]
	v_mfma_f32_16x16x128_f8f6f4 v[132:135], v[18:25], v[238:245], v[132:135]
	v_mfma_f32_16x16x128_f8f6f4 v[136:139], v[26:33], v[238:245], v[136:139]
	s_setprio 0
	s_setprio 1
	v_mfma_f32_16x16x128_f8f6f4 v[128:131], v[10:17], v[202:209], v[128:131]
	v_mfma_f32_16x16x128_f8f6f4 v[124:127], v[2:9], v[202:209], v[124:127]
	v_mfma_f32_16x16x128_f8f6f4 v[116:119], v[2:9], v[222:229], v[116:119]
	v_mfma_f32_16x16x128_f8f6f4 v[120:123], v[10:17], v[222:229], v[120:123]
	v_mfma_f32_16x16x128_f8f6f4 v[112:115], v[10:17], v[230:237], v[112:115]
	v_mfma_f32_16x16x128_f8f6f4 v[108:111], v[2:9], v[230:237], v[108:111]
	v_mfma_f32_16x16x128_f8f6f4 v[100:103], v[2:9], v[238:245], v[100:103]
	v_mfma_f32_16x16x128_f8f6f4 v[104:107], v[10:17], v[238:245], v[104:107]
	s_setprio 0
	s_barrier
	s_add_i32 s64, s64, s40
	s_mov_b64 s[24:25], 0x180
	s_add_i32 s65, s64, 0x2000
	v_lshl_add_u64 v[174:175], v[174:175], 0, s[24:25]
	s_mov_b32 m0, s64
	s_add_u32 s36, s22, 0x20180
	ds_read_b128 v[202:205], v197 offset:49152
	ds_read_b128 v[206:209], v197 offset:50176
	ds_read_b128 v[222:225], v197 offset:51200
	ds_read_b128 v[226:229], v197 offset:52224
	ds_read_b128 v[230:233], v197 offset:53248
	ds_read_b128 v[234:237], v197 offset:54272
	ds_read_b128 v[238:241], v197 offset:55296
	ds_read_b128 v[242:245], v197 offset:56320
	global_load_lds_dwordx4 v[174:175], off
	v_lshl_add_u64 v[174:175], v[190:191], 0, s[24:25]
	s_mov_b32 m0, s65
	s_addc_u32 s37, s23, 0
	s_add_i32 s66, s66, s40
	global_load_lds_dwordx4 v[174:175], off
	v_lshl_add_u64 v[174:175], s[36:37], 0, v[34:35]
	s_mov_b32 m0, s66
	s_add_i32 s67, s66, 0x2000
	global_load_lds_dwordx4 v[174:175], off
	v_lshl_add_u64 v[174:175], s[36:37], 0, v[164:165]
	s_mov_b32 m0, s67
	s_nop 0
	global_load_lds_dwordx4 v[174:175], off
	v_lshl_add_u64 v[174:175], v[192:193], 0, s[24:25]
	s_mov_b32 m0, s47
	s_nop 0
	global_load_lds_dwordx4 v[174:175], off
	v_lshl_add_u64 v[174:175], v[194:195], 0, s[24:25]
	s_mov_b32 m0, s48
	s_nop 0
	global_load_lds_dwordx4 v[174:175], off
	s_waitcnt vmcnt(8)
	s_waitcnt lgkmcnt(0)
	s_barrier
	s_setprio 1
	s_waitcnt lgkmcnt(0)
	v_mfma_f32_16x16x128_f8f6f4 v[96:99], v[26:33], v[202:209], v[96:99]
	v_mfma_f32_16x16x128_f8f6f4 v[92:95], v[18:25], v[202:209], v[92:95]
	v_mfma_f32_16x16x128_f8f6f4 v[84:87], v[18:25], v[222:229], v[84:87]
	v_mfma_f32_16x16x128_f8f6f4 v[88:91], v[26:33], v[222:229], v[88:91]
	v_mfma_f32_16x16x128_f8f6f4 v[80:83], v[26:33], v[230:237], v[80:83]
	v_mfma_f32_16x16x128_f8f6f4 v[76:79], v[18:25], v[230:237], v[76:79]
	v_mfma_f32_16x16x128_f8f6f4 v[68:71], v[18:25], v[238:245], v[68:71]
	v_mfma_f32_16x16x128_f8f6f4 v[72:75], v[26:33], v[238:245], v[72:75]
	s_setprio 0
	s_setprio 1
	v_mfma_f32_16x16x128_f8f6f4 v[64:67], v[10:17], v[202:209], v[64:67]
	v_mfma_f32_16x16x128_f8f6f4 v[60:63], v[2:9], v[202:209], v[60:63]
	v_mfma_f32_16x16x128_f8f6f4 v[52:55], v[2:9], v[222:229], v[52:55]
	v_mfma_f32_16x16x128_f8f6f4 v[56:59], v[10:17], v[222:229], v[56:59]
	v_mfma_f32_16x16x128_f8f6f4 v[48:51], v[10:17], v[230:237], v[48:51]
	v_mfma_f32_16x16x128_f8f6f4 v[44:47], v[2:9], v[230:237], v[44:47]
	v_mfma_f32_16x16x128_f8f6f4 v[36:39], v[2:9], v[238:245], v[36:39]
	v_mfma_f32_16x16x128_f8f6f4 v[40:43], v[10:17], v[238:245], v[40:43]
	s_setprio 0
	s_barrier
	s_add_u32 s30, s30, 0x20180
	s_addc_u32 s31, s31, 0
	s_add_u32 s68, s22, 0x200
	s_addc_u32 s69, s23, 0
	s_mov_b32 s70, 0
	.p2align	6

.LBB0_1159:
	s_mul_i32 s10, s55, 0xb0000
	v_readlane_b32 s16, v254, 4
	v_readlane_b32 s17, v254, 5
	s_add_u32 s10, s16, s10
	s_addc_u32 s11, s17, 0
	s_and_b64 s[16:17], s[4:5], exec
	s_mul_i32 s14, s54, 0xb0000
	s_cselect_b32 s58, s11, s31
	s_cselect_b32 s59, s10, s30
	s_add_u32 s16, s15, s14
	s_addc_u32 s17, s26, 0
	s_and_b64 s[36:37], s[4:5], exec
	s_cselect_b32 s60, s17, s23
	s_cselect_b32 s61, s16, s22
	s_add_u32 s62, s22, 0x100
	v_mov_b32_e32 v36, 0
	s_addc_u32 s63, s23, 0
	s_mov_b32 s64, -2
	v_mov_b32_e32 v37, v36
	v_mov_b32_e32 v38, v36
	v_mov_b32_e32 v39, v36
	v_mov_b32_e32 v40, v36
	v_mov_b32_e32 v41, v36
	v_mov_b32_e32 v42, v36
	v_mov_b32_e32 v43, v36
	v_mov_b32_e32 v48, v36
	v_mov_b32_e32 v49, v36
	v_mov_b32_e32 v50, v36
	v_mov_b32_e32 v51, v36
	v_mov_b32_e32 v56, v36
	v_mov_b32_e32 v57, v36
	v_mov_b32_e32 v58, v36
	v_mov_b32_e32 v59, v36
	v_mov_b32_e32 v64, v36
	v_mov_b32_e32 v65, v36
	v_mov_b32_e32 v66, v36
	v_mov_b32_e32 v67, v36
	v_mov_b32_e32 v72, v36
	v_mov_b32_e32 v73, v36
	v_mov_b32_e32 v74, v36
	v_mov_b32_e32 v75, v36
	v_mov_b32_e32 v80, v36
	v_mov_b32_e32 v81, v36
	v_mov_b32_e32 v82, v36
	v_mov_b32_e32 v83, v36
	v_mov_b32_e32 v88, v36
	v_mov_b32_e32 v89, v36
	v_mov_b32_e32 v90, v36
	v_mov_b32_e32 v91, v36
	v_mov_b32_e32 v44, v36
	v_mov_b32_e32 v45, v36
	v_mov_b32_e32 v46, v36
	v_mov_b32_e32 v47, v36
	v_mov_b32_e32 v52, v36
	v_mov_b32_e32 v53, v36
	v_mov_b32_e32 v54, v36
	v_mov_b32_e32 v55, v36
	v_mov_b32_e32 v60, v36
	v_mov_b32_e32 v61, v36
	v_mov_b32_e32 v62, v36
	v_mov_b32_e32 v63, v36
	v_mov_b32_e32 v68, v36
	v_mov_b32_e32 v69, v36
	v_mov_b32_e32 v70, v36
	v_mov_b32_e32 v71, v36
	v_mov_b32_e32 v76, v36
	v_mov_b32_e32 v77, v36
	v_mov_b32_e32 v78, v36
	v_mov_b32_e32 v79, v36
	v_mov_b32_e32 v84, v36
	v_mov_b32_e32 v85, v36
	v_mov_b32_e32 v86, v36
	v_mov_b32_e32 v87, v36
	v_mov_b32_e32 v92, v36
	v_mov_b32_e32 v93, v36
	v_mov_b32_e32 v94, v36
	v_mov_b32_e32 v95, v36
	v_mov_b32_e32 v96, v36
	v_mov_b32_e32 v97, v36
	v_mov_b32_e32 v98, v36
	v_mov_b32_e32 v99, v36
	v_mov_b32_e32 v100, v36
	v_mov_b32_e32 v101, v36
	v_mov_b32_e32 v102, v36
	v_mov_b32_e32 v103, v36
	v_mov_b32_e32 v104, v36
	v_mov_b32_e32 v105, v36
	v_mov_b32_e32 v106, v36
	v_mov_b32_e32 v107, v36
	v_mov_b32_e32 v112, v36
	v_mov_b32_e32 v113, v36
	v_mov_b32_e32 v114, v36
	v_mov_b32_e32 v115, v36
	v_mov_b32_e32 v120, v36
	v_mov_b32_e32 v121, v36
	v_mov_b32_e32 v122, v36
	v_mov_b32_e32 v123, v36
	v_mov_b32_e32 v128, v36
	v_mov_b32_e32 v129, v36
	v_mov_b32_e32 v130, v36
	v_mov_b32_e32 v131, v36
	v_mov_b32_e32 v136, v36
	v_mov_b32_e32 v137, v36
	v_mov_b32_e32 v138, v36
	v_mov_b32_e32 v139, v36
	v_mov_b32_e32 v148, v36
	v_mov_b32_e32 v149, v36
	v_mov_b32_e32 v150, v36
	v_mov_b32_e32 v151, v36
	v_mov_b32_e32 v152, v36
	v_mov_b32_e32 v153, v36
	v_mov_b32_e32 v154, v36
	v_mov_b32_e32 v155, v36
	v_mov_b32_e32 v108, v36
	v_mov_b32_e32 v109, v36
	v_mov_b32_e32 v110, v36
	v_mov_b32_e32 v111, v36
	v_mov_b32_e32 v116, v36
	v_mov_b32_e32 v117, v36
	v_mov_b32_e32 v118, v36
	v_mov_b32_e32 v119, v36
	v_mov_b32_e32 v124, v36
	v_mov_b32_e32 v125, v36
	v_mov_b32_e32 v126, v36
	v_mov_b32_e32 v127, v36
	v_mov_b32_e32 v132, v36
	v_mov_b32_e32 v133, v36
	v_mov_b32_e32 v134, v36
	v_mov_b32_e32 v135, v36
	v_mov_b32_e32 v140, v36
	v_mov_b32_e32 v141, v36
	v_mov_b32_e32 v142, v36
	v_mov_b32_e32 v143, v36
	v_mov_b32_e32 v144, v36
	v_mov_b32_e32 v145, v36
	v_mov_b32_e32 v146, v36
	v_mov_b32_e32 v147, v36
	v_mov_b32_e32 v156, v36
	v_mov_b32_e32 v157, v36
	v_mov_b32_e32 v158, v36
	v_mov_b32_e32 v159, v36
	v_mov_b32_e32 v160, v36
	v_mov_b32_e32 v161, v36
	v_mov_b32_e32 v162, v36
	v_mov_b32_e32 v163, v36
	.p2align	6
